# K-loops: full 4/4/4/4 LDS-DMA rebalance (As[1][0]@t+3 stage deferred to next iteration's segment 1 via flag s99; As[0][0] before As[0][1] in segment 3)
# speedup vs baseline: 1.0081x; 1.0020x over previous
; #define LAS __attribute__((address_space(3)))
; __device__ __forceinline__ unsigned xb_add(unsigned* p, unsigned v) { return __hip_atomic_fetch_add(p, v, __ATOMIC_RELAXED, __HIP_MEMORY_SCOPE_AGENT); }
; __device__ __forceinline__ unsigned xb_xcc_id() { return (unsigned)__builtin_amdgcn_s_getreg((3 << 11) | 20) & 0xFu; }
; __device__ __forceinline__ XcdBarrier xcd_barrier_post(unsigned* bar, volatile LAS unsigned* st) {
;     XcdBarrier b; b.bar = bar; b.x = xb_xcc_id(); b.st = st;
;     if (threadIdx.x == 0) (void)xb_add(&bar[XB_XCNT(b.x)], 1u);
;     return b;
; __global__ void __launch_bounds__(512, 2) mk_fwd(Params P) {
;     extern __shared__ __attribute__((aligned(16))) unsigned char lds_raw[];
;     LAS unsigned char* lds = (LAS unsigned char*)lds_raw;
;     const int tid = threadIdx.x, lane = tid & 63, wave = __builtin_amdgcn_readfirstlane(tid >> 6);
;     const int lo = P.ph_lo, hi = P.ph_hi, G = gridDim.x, bx = blockIdx.x;
;     unsigned char* ws = P.ws;
;     const int gw = bx * NW + wave, NGW = G * NW;
;     ...
;     volatile LAS unsigned* xst = (volatile LAS unsigned*)(lds + LDS_BYTES - 16);
;     if (tid < 4) xst[tid] = 0u;
;     __syncthreads();
;     const XcdBarrier bar = xcd_barrier_post((unsigned*)(ws + WS_BAR), xst);
_Z6mk_fwd6Params:
	s_mov_b32 s99, 0
	s_load_dwordx2 s[64:65], s[0:1], 0xa8
	s_load_dword s68, s[0:1], 0xb8
	s_mov_b64 s[94:95], s[0:1]
	s_add_u32 s0, s94, 0xb8
	s_addc_u32 s1, s95, 0
	v_readfirstlane_b32 s56, v0
	v_writelane_b32 v254, s0, 0
	v_cmp_gt_u32_e32 vcc, 4, v0
	s_nop 0
	v_writelane_b32 v254, s1, 1
	s_and_saveexec_b64 s[4:5], vcc
	v_lshl_add_u32 v1, v0, 2, 0
	v_add_u32_e32 v1, 0x253f0, v1
	v_mov_b32_e32 v2, 0
	ds_write_b32 v1, v2
	s_or_b64 exec, exec, s[4:5]
	s_waitcnt lgkmcnt(0)
	s_barrier
	s_getreg_b32 s0, hwreg(HW_REG_XCC_ID, 0, 4)
	s_and_b32 s0, s0, 15
	v_writelane_b32 v254, s0, 2
	v_cmp_eq_u32_e64 s[0:1], 0, v0
	s_nop 1
	v_writelane_b32 v254, s0, 3
	s_nop 1
	v_writelane_b32 v254, s1, 4
	s_and_saveexec_b64 s[4:5], s[0:1]
	s_cbranch_execz .LBB0_5
	s_mov_b64 s[6:7], exec
	v_mbcnt_lo_u32_b32 v1, s6, 0
	v_mbcnt_hi_u32_b32 v1, s7, v1
	v_cmp_eq_u32_e32 vcc, 0, v1
	s_and_b64 s[8:9], exec, vcc
	s_mov_b64 exec, s[8:9]
	s_cbranch_execz .LBB0_5
	v_readlane_b32 s0, v254, 2
	s_lshl_b32 s0, s0, 8
	s_bcnt1_i32_b64 s1, s[6:7]
	v_mov_b32_e32 v1, s0
	v_mov_b32_e32 v2, s1
	global_atomic_add v1, v2, s[64:65] offset:1024

; #define PG8_STAGE(bufoff, gbase, voff) do { _Pragma("unroll") for (int _i = 0; _i < 2; ++_i) \
;         __builtin_amdgcn_global_load_lds((const unsigned*)((const char*)(gbase) + (voff)[_i]), (PG8_LAS unsigned*)(lds + (bufoff) + ldsw + _i * 8192), 16, 0, 0); } while (0)
; #define PG8_LDA(dst, b, h) do { _Pragma("unroll") for (int m = 0; m < 4; ++m) { const bf16x8 f0_ = *(const PG8_LAS bf16x8*)(lds + PG8_SA(b, h) + aoff + m * 2048), f1_ = *(const PG8_LAS bf16x8*)(lds + PG8_SA(b, h) + aoff + m * 2048 + 1024); dst[m].set(f0_, f1_); } } while (0)
; #define PG8_LDB(dst, b, h) do { _Pragma("unroll") for (int n = 0; n < 2; ++n) { const bf16x8 f0_ = *(const PG8_LAS bf16x8*)(lds + PG8_SB(b, h) + boff + n * 2048), f1_ = *(const PG8_LAS bf16x8*)(lds + PG8_SB(b, h) + boff + n * 2048 + 1024); dst[n].set(f0_, f1_); } } while (0)
; #define PG8_WAIT_V(n) asm volatile("s_waitcnt vmcnt(" #n ")" ::: "memory")
; #define PG8_WAIT_L(n) asm volatile("s_waitcnt lgkmcnt(" #n ")" ::: "memory")
; #define PG8_BAR __builtin_amdgcn_s_barrier()
; #define PG8_SCHED __builtin_amdgcn_sched_barrier(0)
; template <class Epi, class Sched, bool ALIGN_EPI = false, bool SP2 = false>
; __device__ __forceinline__ void gemm_phase(PG8_LAS unsigned char* lds, const Gemm g, const Sched& S, const Epi& E) {
;     ...
;             const bool last = (t == nt - 2);
;             const char* a1 = cA + (size_t)(t + 1) * kstep;
;             const char* a2 = last ? nA : cA + (size_t)(t + 2) * kstep; const char* b2 = last ? nB : cB + (size_t)(t + 2) * kstep;
;             const char* a3 = a2 + kstep; const char* b3 = b2 + kstep;
;             if (last && has_next) S.a_ready(nxt);
;             if constexpr (SP2) {
;             PG8_LDB(B0, 0, 0); PG8_LDB(B1, 0, 1); PG8_SCHED; PG8_LDA(At, 0, 0); PG8_STAGE(PG8_SA(1, 1), a1 + hstep, voffA);
;             PG8_WAIT_V(8); PG8_WAIT_L(0); PG8_BAR; PG8_MMA(0, 0, At, B0); PG8_MMA(0, 1, At, B1); PG8_BAR; PG8_SCHED;
;             PG8_LDA(At, 0, 1); PG8_STAGE(PG8_SB(0, 0), b2, voffB); PG8_STAGE(PG8_SB(0, 1), b2 + hstepB, voffB); PG8_STAGE(PG8_SA(0, 0), a2, voffA);
;             PG8_WAIT_V(8); PG8_WAIT_L(0); PG8_BAR; PG8_MMA(1, 0, At, B0); PG8_MMA(1, 1, At, B1); PG8_BAR; PG8_SCHED;
.LBB0_204:
	ds_read_b128 v[18:21], v203
	ds_read_b128 v[22:25], v203 offset:1024
	ds_read_b128 v[26:29], v203 offset:2048
	ds_read_b128 v[30:33], v203 offset:3072
	ds_read_b128 v[2:5], v204
	ds_read_b128 v[6:9], v204 offset:1024
	ds_read_b128 v[10:13], v204 offset:2048
	ds_read_b128 v[14:17], v204 offset:3072
	s_add_i32 s53, s48, 2
	s_add_u32 s0, s2, 0x80
	s_addc_u32 s1, s3, 0
	s_cmp_eq_u32 s71, s48
	s_cselect_b32 s48, s44, s0
	s_cselect_b32 s49, s45, s1
	s_cselect_b32 s51, s47, s52
	s_cselect_b32 s50, s46, s20
	s_cmp_eq_u32 s99, 0
	s_cbranch_scc1 .Lkr0_a
	v_lshl_add_u64 v[190:191], v[190:191], 0, s[36:37]
	s_mov_b32 m0, s66
	v_lshl_add_u64 v[192:193], v[192:193], 0, s[36:37]
	global_load_lds_dwordx4 v[190:191], off
	s_mov_b32 m0, s67
	s_nop 0
	global_load_lds_dwordx4 v[192:193], off
.Lkr0_a:
	v_lshl_add_u64 v[190:191], s[2:3], 0, v[174:175]
	s_add_i32 m0, s58, 0xc000
	ds_read_b128 v[182:185], v205
	ds_read_b128 v[186:189], v205 offset:1024
	ds_read_b128 v[212:215], v205 offset:2048
	ds_read_b128 v[216:219], v205 offset:3072
	ds_read_b128 v[220:223], v205 offset:4096
	ds_read_b128 v[224:227], v205 offset:5120
	ds_read_b128 v[228:231], v205 offset:6144
	ds_read_b128 v[232:235], v205 offset:7168
	global_load_lds_dwordx4 v[190:191], off
	v_lshl_add_u64 v[190:191], s[2:3], 0, v[176:177]
	s_add_i32 m0, s58, 0xe000
	s_nop 0
	global_load_lds_dwordx4 v[190:191], off
	s_waitcnt vmcnt(8)
	s_waitcnt lgkmcnt(0)
	s_barrier
	s_setprio 1
	s_waitcnt lgkmcnt(0)
	v_mfma_scale_f32_16x16x128_f8f6f4 v[158:161], v[18:25], v[182:189], v[158:161], v206, v207 op_sel_hi:[0,0,0]
	v_mfma_scale_f32_16x16x128_f8f6f4 v[154:157], v[26:33], v[182:189], v[154:157], v206, v207 op_sel_hi:[0,0,0]
	v_mfma_scale_f32_16x16x128_f8f6f4 v[142:145], v[18:25], v[212:219], v[142:145], v206, v207 op_sel_hi:[0,0,0]
	v_mfma_scale_f32_16x16x128_f8f6f4 v[138:141], v[26:33], v[212:219], v[138:141], v206, v207 op_sel_hi:[0,0,0]
	v_mfma_scale_f32_16x16x128_f8f6f4 v[126:129], v[18:25], v[220:227], v[126:129], v206, v207 op_sel_hi:[0,0,0]
	v_mfma_scale_f32_16x16x128_f8f6f4 v[122:125], v[26:33], v[220:227], v[122:125], v206, v207 op_sel_hi:[0,0,0]
	v_mfma_scale_f32_16x16x128_f8f6f4 v[110:113], v[18:25], v[228:235], v[110:113], v206, v207 op_sel_hi:[0,0,0]
	v_mfma_scale_f32_16x16x128_f8f6f4 v[106:109], v[26:33], v[228:235], v[106:109], v206, v207 op_sel_hi:[0,0,0]
	s_setprio 0
	s_setprio 1
	v_mfma_scale_f32_16x16x128_f8f6f4 v[150:153], v[2:9], v[182:189], v[150:153], v206, v207 op_sel_hi:[0,0,0]
	v_mfma_scale_f32_16x16x128_f8f6f4 v[146:149], v[10:17], v[182:189], v[146:149], v206, v207 op_sel_hi:[0,0,0]
	v_mfma_scale_f32_16x16x128_f8f6f4 v[134:137], v[2:9], v[212:219], v[134:137], v206, v207 op_sel_hi:[0,0,0]
	v_mfma_scale_f32_16x16x128_f8f6f4 v[130:133], v[10:17], v[212:219], v[130:133], v206, v207 op_sel_hi:[0,0,0]
	v_mfma_scale_f32_16x16x128_f8f6f4 v[118:121], v[2:9], v[220:227], v[118:121], v206, v207 op_sel_hi:[0,0,0]
	v_mfma_scale_f32_16x16x128_f8f6f4 v[114:117], v[10:17], v[220:227], v[114:117], v206, v207 op_sel_hi:[0,0,0]
	v_mfma_scale_f32_16x16x128_f8f6f4 v[102:105], v[2:9], v[228:235], v[102:105], v206, v207 op_sel_hi:[0,0,0]
	v_mfma_scale_f32_16x16x128_f8f6f4 v[98:101], v[10:17], v[228:235], v[98:101], v206, v207 op_sel_hi:[0,0,0]
	s_setprio 0
	s_barrier
	s_add_i32 s0, s76, s57
	v_lshl_add_u64 v[182:183], s[50:51], 0, v[164:165]
	s_mov_b32 m0, s0
	ds_read_b128 v[212:215], v205 offset:16384
	ds_read_b128 v[216:219], v205 offset:17408
	ds_read_b128 v[220:223], v205 offset:18432
	ds_read_b128 v[224:227], v205 offset:19456
	ds_read_b128 v[228:231], v205 offset:20480
	ds_read_b128 v[232:235], v205 offset:21504
	ds_read_b128 v[236:239], v205 offset:22528
	ds_read_b128 v[240:243], v205 offset:23552
	global_load_lds_dwordx4 v[182:183], off
	s_add_i32 m0, s0, 0x2000
	v_lshl_add_u64 v[184:185], s[50:51], 0, v[168:169]
	s_add_u32 s50, s50, s16
	s_addc_u32 s51, s51, s17
	s_add_i32 s0, s77, s57
	global_load_lds_dwordx4 v[184:185], off
	v_lshl_add_u64 v[186:187], s[50:51], 0, v[164:165]
	s_mov_b32 m0, s0
	v_lshl_add_u64 v[188:189], s[50:51], 0, v[168:169]
	global_load_lds_dwordx4 v[186:187], off
	s_add_i32 m0, s0, 0x2000
	v_lshl_add_u64 v[190:191], s[48:49], 0, v[162:163]
	global_load_lds_dwordx4 v[188:189], off
	v_lshl_add_u64 v[192:193], s[48:49], 0, v[166:167]
	s_waitcnt vmcnt(6)
	s_waitcnt lgkmcnt(0)
	s_barrier
	s_setprio 1
	s_waitcnt lgkmcnt(0)
	v_mfma_scale_f32_16x16x128_f8f6f4 v[94:97], v[18:25], v[212:219], v[94:97], v206, v207 op_sel_hi:[0,0,0]
	v_mfma_scale_f32_16x16x128_f8f6f4 v[90:93], v[26:33], v[212:219], v[90:93], v206, v207 op_sel_hi:[0,0,0]
	v_mfma_scale_f32_16x16x128_f8f6f4 v[78:81], v[18:25], v[220:227], v[78:81], v206, v207 op_sel_hi:[0,0,0]
	v_mfma_scale_f32_16x16x128_f8f6f4 v[74:77], v[26:33], v[220:227], v[74:77], v206, v207 op_sel_hi:[0,0,0]
	v_mfma_scale_f32_16x16x128_f8f6f4 v[62:65], v[18:25], v[228:235], v[62:65], v206, v207 op_sel_hi:[0,0,0]
	v_mfma_scale_f32_16x16x128_f8f6f4 v[58:61], v[26:33], v[228:235], v[58:61], v206, v207 op_sel_hi:[0,0,0]
	v_mfma_scale_f32_16x16x128_f8f6f4 v[46:49], v[18:25], v[236:243], v[46:49], v206, v207 op_sel_hi:[0,0,0]
	v_mfma_scale_f32_16x16x128_f8f6f4 v[42:45], v[26:33], v[236:243], v[42:45], v206, v207 op_sel_hi:[0,0,0]
	s_setprio 0
	s_setprio 1
	v_mfma_scale_f32_16x16x128_f8f6f4 v[86:89], v[2:9], v[212:219], v[86:89], v206, v207 op_sel_hi:[0,0,0]
	v_mfma_scale_f32_16x16x128_f8f6f4 v[82:85], v[10:17], v[212:219], v[82:85], v206, v207 op_sel_hi:[0,0,0]
	v_mfma_scale_f32_16x16x128_f8f6f4 v[70:73], v[2:9], v[220:227], v[70:73], v206, v207 op_sel_hi:[0,0,0]
	v_mfma_scale_f32_16x16x128_f8f6f4 v[66:69], v[10:17], v[220:227], v[66:69], v206, v207 op_sel_hi:[0,0,0]
	v_mfma_scale_f32_16x16x128_f8f6f4 v[54:57], v[2:9], v[228:235], v[54:57], v206, v207 op_sel_hi:[0,0,0]
	v_mfma_scale_f32_16x16x128_f8f6f4 v[50:53], v[10:17], v[228:235], v[50:53], v206, v207 op_sel_hi:[0,0,0]
	v_mfma_scale_f32_16x16x128_f8f6f4 v[38:41], v[2:9], v[236:243], v[38:41], v206, v207 op_sel_hi:[0,0,0]
	v_mfma_scale_f32_16x16x128_f8f6f4 v[34:37], v[10:17], v[236:243], v[34:37], v206, v207 op_sel_hi:[0,0,0]
	s_setprio 0
	s_barrier
; #define PG8_STAGE(bufoff, gbase, voff) do { _Pragma("unroll") for (int _i = 0; _i < 2; ++_i) \
;         __builtin_amdgcn_global_load_lds((const unsigned*)((const char*)(gbase) + (voff)[_i]), (PG8_LAS unsigned*)(lds + (bufoff) + ldsw + _i * 8192), 16, 0, 0); } while (0)
; #define PG8_LDA(dst, b, h) do { _Pragma("unroll") for (int m = 0; m < 4; ++m) { const bf16x8 f0_ = *(const PG8_LAS bf16x8*)(lds + PG8_SA(b, h) + aoff + m * 2048), f1_ = *(const PG8_LAS bf16x8*)(lds + PG8_SA(b, h) + aoff + m * 2048 + 1024); dst[m].set(f0_, f1_); } } while (0)
; #define PG8_LDB(dst, b, h) do { _Pragma("unroll") for (int n = 0; n < 2; ++n) { const bf16x8 f0_ = *(const PG8_LAS bf16x8*)(lds + PG8_SB(b, h) + boff + n * 2048), f1_ = *(const PG8_LAS bf16x8*)(lds + PG8_SB(b, h) + boff + n * 2048 + 1024); dst[n].set(f0_, f1_); } } while (0)
; #define PG8_WAIT_V(n) asm volatile("s_waitcnt vmcnt(" #n ")" ::: "memory")
; #define PG8_WAIT_L(n) asm volatile("s_waitcnt lgkmcnt(" #n ")" ::: "memory")
; #define PG8_BAR __builtin_amdgcn_s_barrier()
; #define PG8_SCHED __builtin_amdgcn_sched_barrier(0)
; template <class Epi, class Sched, bool ALIGN_EPI = false, bool SP2 = false>
; __device__ __forceinline__ void gemm_phase(PG8_LAS unsigned char* lds, const Gemm g, const Sched& S, const Epi& E) {
;     ...
;             PG8_LDB(B0, 1, 0); PG8_LDB(B1, 1, 1); PG8_SCHED; PG8_LDA(At, 1, 0); PG8_STAGE(PG8_SA(0, 1), a2 + hstep, voffA);
;             PG8_WAIT_V(8); PG8_WAIT_L(0); PG8_BAR; PG8_MMA(0, 0, At, B0); PG8_MMA(0, 1, At, B1); PG8_BAR; PG8_SCHED;
;             PG8_LDA(At, 1, 1); PG8_STAGE(PG8_SB(1, 0), b3, voffB); PG8_STAGE(PG8_SB(1, 1), b3 + hstepB, voffB); PG8_STAGE(PG8_SA(1, 0), a3, voffA);
;             PG8_WAIT_V(8); PG8_WAIT_L(0); PG8_BAR; PG8_MMA(1, 0, At, B0); PG8_MMA(1, 1, At, B1); PG8_BAR; PG8_SCHED;
	s_add_i32 s0, 0, 0x18000
	s_add_i32 s1, 0, 0x1c000
	v_add_u32_e32 v14, s0, v194
	v_add_u32_e32 v30, s1, v194
	ds_read_b128 v[2:5], v14
	ds_read_b128 v[6:9], v14 offset:1024
	ds_read_b128 v[10:13], v14 offset:2048
	ds_read_b128 v[14:17], v14 offset:3072
	ds_read_b128 v[18:21], v30
	ds_read_b128 v[22:25], v30 offset:1024
	ds_read_b128 v[26:29], v30 offset:2048
	ds_read_b128 v[30:33], v30 offset:3072
	s_add_u32 s48, s48, s14
	s_addc_u32 s49, s49, s15
	s_mov_b32 m0, s61
	v_lshl_add_u64 v[244:245], s[48:49], 0, v[162:163]
	ds_read_b128 v[212:215], v205 offset:32768
	ds_read_b128 v[216:219], v205 offset:33792
	ds_read_b128 v[220:223], v205 offset:34816
	ds_read_b128 v[224:227], v205 offset:35840
	ds_read_b128 v[228:231], v205 offset:36864
	ds_read_b128 v[232:235], v205 offset:37888
	ds_read_b128 v[236:239], v205 offset:38912
	ds_read_b128 v[240:243], v205 offset:39936
	s_mov_b32 m0, s58
	s_nop 0
	global_load_lds_dwordx4 v[190:191], off
	s_mov_b32 m0, s59
	s_nop 0
	global_load_lds_dwordx4 v[192:193], off
	s_mov_b32 m0, s61
	s_nop 0
	global_load_lds_dwordx4 v[244:245], off
	v_lshl_add_u64 v[244:245], s[48:49], 0, v[166:167]
	s_mov_b32 m0, s63
	s_nop 0
	global_load_lds_dwordx4 v[244:245], off
	s_waitcnt vmcnt(8)
	s_waitcnt lgkmcnt(0)
	s_barrier
	s_setprio 1
	s_waitcnt lgkmcnt(0)
	v_mfma_scale_f32_16x16x128_f8f6f4 v[158:161], v[2:9], v[212:219], v[158:161], v206, v207 op_sel_hi:[0,0,0]
	v_mfma_scale_f32_16x16x128_f8f6f4 v[154:157], v[10:17], v[212:219], v[154:157], v206, v207 op_sel_hi:[0,0,0]
	v_mfma_scale_f32_16x16x128_f8f6f4 v[142:145], v[2:9], v[220:227], v[142:145], v206, v207 op_sel_hi:[0,0,0]
	v_mfma_scale_f32_16x16x128_f8f6f4 v[138:141], v[10:17], v[220:227], v[138:141], v206, v207 op_sel_hi:[0,0,0]
	v_mfma_scale_f32_16x16x128_f8f6f4 v[126:129], v[2:9], v[228:235], v[126:129], v206, v207 op_sel_hi:[0,0,0]
	v_mfma_scale_f32_16x16x128_f8f6f4 v[122:125], v[10:17], v[228:235], v[122:125], v206, v207 op_sel_hi:[0,0,0]
	v_mfma_scale_f32_16x16x128_f8f6f4 v[110:113], v[2:9], v[236:243], v[110:113], v206, v207 op_sel_hi:[0,0,0]
	v_mfma_scale_f32_16x16x128_f8f6f4 v[106:109], v[10:17], v[236:243], v[106:109], v206, v207 op_sel_hi:[0,0,0]
	s_setprio 0
	s_setprio 1
	v_mfma_scale_f32_16x16x128_f8f6f4 v[150:153], v[18:25], v[212:219], v[150:153], v206, v207 op_sel_hi:[0,0,0]
	v_mfma_scale_f32_16x16x128_f8f6f4 v[146:149], v[26:33], v[212:219], v[146:149], v206, v207 op_sel_hi:[0,0,0]
	v_mfma_scale_f32_16x16x128_f8f6f4 v[134:137], v[18:25], v[220:227], v[134:137], v206, v207 op_sel_hi:[0,0,0]
	v_mfma_scale_f32_16x16x128_f8f6f4 v[130:133], v[26:33], v[220:227], v[130:133], v206, v207 op_sel_hi:[0,0,0]
	v_mfma_scale_f32_16x16x128_f8f6f4 v[118:121], v[18:25], v[228:235], v[118:121], v206, v207 op_sel_hi:[0,0,0]
	v_mfma_scale_f32_16x16x128_f8f6f4 v[114:117], v[26:33], v[228:235], v[114:117], v206, v207 op_sel_hi:[0,0,0]
	v_mfma_scale_f32_16x16x128_f8f6f4 v[102:105], v[18:25], v[236:243], v[102:105], v206, v207 op_sel_hi:[0,0,0]
	v_mfma_scale_f32_16x16x128_f8f6f4 v[98:101], v[26:33], v[236:243], v[98:101], v206, v207 op_sel_hi:[0,0,0]
	s_setprio 0
	s_barrier
	s_add_i32 s0, s0, s57
	v_lshl_add_u64 v[182:183], v[182:183], 0, s[36:37]
	s_mov_b32 m0, s0
	ds_read_b128 v[212:215], v205 offset:49152
	ds_read_b128 v[216:219], v205 offset:50176
	ds_read_b128 v[220:223], v205 offset:51200
	ds_read_b128 v[224:227], v205 offset:52224
	ds_read_b128 v[228:231], v205 offset:53248
	ds_read_b128 v[232:235], v205 offset:54272
	ds_read_b128 v[236:239], v205 offset:55296
	ds_read_b128 v[240:243], v205 offset:56320
	global_load_lds_dwordx4 v[182:183], off
	v_lshl_add_u64 v[182:183], v[184:185], 0, s[36:37]
	s_add_i32 m0, s0, 0x2000
	s_add_i32 s0, s1, s57
	global_load_lds_dwordx4 v[182:183], off
	v_lshl_add_u64 v[182:183], v[186:187], 0, s[36:37]
	s_mov_b32 m0, s0
	s_nop 0
	global_load_lds_dwordx4 v[182:183], off
	v_lshl_add_u64 v[182:183], v[188:189], 0, s[36:37]
	s_add_i32 m0, s0, 0x2000
	s_nop 0
	global_load_lds_dwordx4 v[182:183], off
	s_cmp_ge_i32 s53, s69
	s_cbranch_scc0 .Lkr0_b
	v_lshl_add_u64 v[182:183], v[190:191], 0, s[36:37]
	s_mov_b32 m0, s66
	s_nop 0
	global_load_lds_dwordx4 v[182:183], off
	v_lshl_add_u64 v[182:183], v[192:193], 0, s[36:37]
	s_mov_b32 m0, s67
	s_nop 0
	global_load_lds_dwordx4 v[182:183], off
.Lkr0_b:
	s_waitcnt vmcnt(6)
	s_waitcnt lgkmcnt(0)
	s_barrier
	s_setprio 1
	s_waitcnt lgkmcnt(0)
	v_mfma_scale_f32_16x16x128_f8f6f4 v[94:97], v[2:9], v[212:219], v[94:97], v206, v207 op_sel_hi:[0,0,0]
	v_mfma_scale_f32_16x16x128_f8f6f4 v[90:93], v[10:17], v[212:219], v[90:93], v206, v207 op_sel_hi:[0,0,0]
	v_mfma_scale_f32_16x16x128_f8f6f4 v[78:81], v[2:9], v[220:227], v[78:81], v206, v207 op_sel_hi:[0,0,0]
	v_mfma_scale_f32_16x16x128_f8f6f4 v[74:77], v[10:17], v[220:227], v[74:77], v206, v207 op_sel_hi:[0,0,0]
	v_mfma_scale_f32_16x16x128_f8f6f4 v[62:65], v[2:9], v[228:235], v[62:65], v206, v207 op_sel_hi:[0,0,0]
	v_mfma_scale_f32_16x16x128_f8f6f4 v[58:61], v[10:17], v[228:235], v[58:61], v206, v207 op_sel_hi:[0,0,0]
	v_mfma_scale_f32_16x16x128_f8f6f4 v[46:49], v[2:9], v[236:243], v[46:49], v206, v207 op_sel_hi:[0,0,0]
	v_mfma_scale_f32_16x16x128_f8f6f4 v[42:45], v[10:17], v[236:243], v[42:45], v206, v207 op_sel_hi:[0,0,0]
	s_setprio 0
	s_setprio 1
	v_mfma_scale_f32_16x16x128_f8f6f4 v[86:89], v[18:25], v[212:219], v[86:89], v206, v207 op_sel_hi:[0,0,0]
	v_mfma_scale_f32_16x16x128_f8f6f4 v[82:85], v[26:33], v[212:219], v[82:85], v206, v207 op_sel_hi:[0,0,0]
	v_mfma_scale_f32_16x16x128_f8f6f4 v[70:73], v[18:25], v[220:227], v[70:73], v206, v207 op_sel_hi:[0,0,0]
	v_mfma_scale_f32_16x16x128_f8f6f4 v[66:69], v[26:33], v[220:227], v[66:69], v206, v207 op_sel_hi:[0,0,0]
	v_mfma_scale_f32_16x16x128_f8f6f4 v[54:57], v[18:25], v[228:235], v[54:57], v206, v207 op_sel_hi:[0,0,0]
	v_mfma_scale_f32_16x16x128_f8f6f4 v[50:53], v[26:33], v[228:235], v[50:53], v206, v207 op_sel_hi:[0,0,0]
	v_mfma_scale_f32_16x16x128_f8f6f4 v[38:41], v[18:25], v[236:243], v[38:41], v206, v207 op_sel_hi:[0,0,0]
	v_mfma_scale_f32_16x16x128_f8f6f4 v[34:37], v[26:33], v[236:243], v[34:37], v206, v207 op_sel_hi:[0,0,0]
	s_setprio 0
	s_barrier
	s_add_u32 s2, s2, 0x100
	s_addc_u32 s3, s3, 0
	s_add_u32 s20, s20, 0x100
	s_addc_u32 s52, s52, 0
	s_cmp_ge_i32 s53, s69
	s_cselect_b32 s99, 0, 1
	s_mov_b32 s48, s53
	s_cbranch_scc0 .LBB0_204

; #define PG8_STAGE(bufoff, gbase, voff) do { _Pragma("unroll") for (int _i = 0; _i < 2; ++_i) \
;         __builtin_amdgcn_global_load_lds((const unsigned*)((const char*)(gbase) + (voff)[_i]), (PG8_LAS unsigned*)(lds + (bufoff) + ldsw + _i * 8192), 16, 0, 0); } while (0)
; #define PG8_LDA(dst, b, h) do { _Pragma("unroll") for (int m = 0; m < 4; ++m) { const bf16x8 f0_ = *(const PG8_LAS bf16x8*)(lds + PG8_SA(b, h) + aoff + m * 2048), f1_ = *(const PG8_LAS bf16x8*)(lds + PG8_SA(b, h) + aoff + m * 2048 + 1024); dst[m].set(f0_, f1_); } } while (0)
; #define PG8_LDB(dst, b, h) do { _Pragma("unroll") for (int n = 0; n < 2; ++n) { const bf16x8 f0_ = *(const PG8_LAS bf16x8*)(lds + PG8_SB(b, h) + boff + n * 2048), f1_ = *(const PG8_LAS bf16x8*)(lds + PG8_SB(b, h) + boff + n * 2048 + 1024); dst[n].set(f0_, f1_); } } while (0)
; #define PG8_WAIT_V(n) asm volatile("s_waitcnt vmcnt(" #n ")" ::: "memory")
; #define PG8_WAIT_L(n) asm volatile("s_waitcnt lgkmcnt(" #n ")" ::: "memory")
; #define PG8_BAR __builtin_amdgcn_s_barrier()
; #define PG8_SCHED __builtin_amdgcn_sched_barrier(0)
; template <class Epi, class Sched, bool ALIGN_EPI = false, bool SP2 = false>
; __device__ __forceinline__ void gemm_phase(PG8_LAS unsigned char* lds, const Gemm g, const Sched& S, const Epi& E) {
;     ...
;             const bool last = (t == nt - 2);
;             const char* a1 = cA + (size_t)(t + 1) * kstep;
;             const char* a2 = last ? nA : cA + (size_t)(t + 2) * kstep; const char* b2 = last ? nB : cB + (size_t)(t + 2) * kstep;
;             const char* a3 = a2 + kstep; const char* b3 = b2 + kstep;
;             if (last && has_next) S.a_ready(nxt);
;             if constexpr (SP2) {
;             PG8_LDB(B0, 0, 0); PG8_LDB(B1, 0, 1); PG8_SCHED; PG8_LDA(At, 0, 0); PG8_STAGE(PG8_SA(1, 1), a1 + hstep, voffA);
;             PG8_WAIT_V(8); PG8_WAIT_L(0); PG8_BAR; PG8_MMA(0, 0, At, B0); PG8_MMA(0, 1, At, B1); PG8_BAR; PG8_SCHED;
;             PG8_LDA(At, 0, 1); PG8_STAGE(PG8_SB(0, 0), b2, voffB); PG8_STAGE(PG8_SB(0, 1), b2 + hstepB, voffB); PG8_STAGE(PG8_SA(0, 0), a2, voffA);
;             PG8_WAIT_V(8); PG8_WAIT_L(0); PG8_BAR; PG8_MMA(1, 0, At, B0); PG8_MMA(1, 1, At, B1); PG8_BAR; PG8_SCHED;
.LBB0_984:
	s_add_i32 s75, s42, 2
	v_add_u32_e32 v186, s59, v173
	v_add_u32_e32 v202, s61, v173
	s_add_u32 s0, s38, s40
	ds_read_b128 v[168:171], v186
	ds_read_b128 v[178:181], v186 offset:1024
	ds_read_b128 v[182:185], v186 offset:2048
	ds_read_b128 v[186:189], v186 offset:3072
	ds_read_b128 v[190:193], v202
	ds_read_b128 v[194:197], v202 offset:1024
	ds_read_b128 v[198:201], v202 offset:2048
	ds_read_b128 v[202:205], v202 offset:3072
	s_addc_u32 s1, s39, s41
	s_add_u32 s0, s0, 0x100
	s_addc_u32 s1, s1, 0
	s_add_u32 s33, s73, s40
	s_addc_u32 s76, s74, s41
	s_cmp_eq_u32 s57, s42
	s_cselect_b32 s43, s3, s1
	s_cselect_b32 s42, s2, s0
	s_cselect_b32 s1, s37, s76
	s_cselect_b32 s0, s36, s33
	v_lshl_add_u64 v[240:241], v[164:165], 0, s[40:41]
	s_add_i32 m0, s47, 0xc000
	ds_read_b128 v[206:209], v176
	ds_read_b128 v[212:215], v176 offset:1024
	ds_read_b128 v[216:219], v176 offset:2048
	ds_read_b128 v[220:223], v176 offset:3072
	ds_read_b128 v[224:227], v176 offset:4096
	ds_read_b128 v[228:231], v176 offset:5120
	ds_read_b128 v[232:235], v176 offset:6144
	ds_read_b128 v[236:239], v176 offset:7168
	global_load_lds_dwordx4 v[240:241], off
	v_lshl_add_u64 v[240:241], v[166:167], 0, s[40:41]
	s_add_i32 m0, s47, 0xe000
	s_nop 0
	global_load_lds_dwordx4 v[240:241], off
	s_waitcnt vmcnt(8)
	s_waitcnt lgkmcnt(0)
	s_barrier
	s_setprio 1
	s_waitcnt lgkmcnt(0)
	v_mfma_f32_16x16x32_bf16 v[126:129], v[168:171], v[206:209], v[126:129]
	v_mfma_f32_16x16x32_bf16 v[122:125], v[182:185], v[206:209], v[122:125]
	v_mfma_f32_16x16x32_bf16 v[110:113], v[168:171], v[216:219], v[110:113]
	v_mfma_f32_16x16x32_bf16 v[106:109], v[182:185], v[216:219], v[106:109]
	v_mfma_f32_16x16x32_bf16 v[94:97], v[168:171], v[224:227], v[94:97]
	v_mfma_f32_16x16x32_bf16 v[90:93], v[182:185], v[224:227], v[90:93]
	v_mfma_f32_16x16x32_bf16 v[78:81], v[168:171], v[232:235], v[78:81]
	v_mfma_f32_16x16x32_bf16 v[74:77], v[182:185], v[232:235], v[74:77]
	v_mfma_f32_16x16x32_bf16 v[126:129], v[178:181], v[212:215], v[126:129]
	v_mfma_f32_16x16x32_bf16 v[122:125], v[186:189], v[212:215], v[122:125]
	v_mfma_f32_16x16x32_bf16 v[110:113], v[178:181], v[220:223], v[110:113]
	v_mfma_f32_16x16x32_bf16 v[106:109], v[186:189], v[220:223], v[106:109]
	v_mfma_f32_16x16x32_bf16 v[94:97], v[178:181], v[228:231], v[94:97]
	v_mfma_f32_16x16x32_bf16 v[90:93], v[186:189], v[228:231], v[90:93]
	v_mfma_f32_16x16x32_bf16 v[78:81], v[178:181], v[236:239], v[78:81]
	v_mfma_f32_16x16x32_bf16 v[74:77], v[186:189], v[236:239], v[74:77]
	s_setprio 0
	s_setprio 1
	v_mfma_f32_16x16x32_bf16 v[118:121], v[190:193], v[206:209], v[118:121]
	v_mfma_f32_16x16x32_bf16 v[114:117], v[198:201], v[206:209], v[114:117]
	v_mfma_f32_16x16x32_bf16 v[102:105], v[190:193], v[216:219], v[102:105]
	v_mfma_f32_16x16x32_bf16 v[98:101], v[198:201], v[216:219], v[98:101]
	v_mfma_f32_16x16x32_bf16 v[86:89], v[190:193], v[224:227], v[86:89]
	v_mfma_f32_16x16x32_bf16 v[82:85], v[198:201], v[224:227], v[82:85]
	v_mfma_f32_16x16x32_bf16 v[70:73], v[190:193], v[232:235], v[70:73]
	v_mfma_f32_16x16x32_bf16 v[66:69], v[198:201], v[232:235], v[66:69]
	v_mfma_f32_16x16x32_bf16 v[118:121], v[194:197], v[212:215], v[118:121]
	v_mfma_f32_16x16x32_bf16 v[114:117], v[202:205], v[212:215], v[114:117]
	v_mfma_f32_16x16x32_bf16 v[102:105], v[194:197], v[220:223], v[102:105]
	v_mfma_f32_16x16x32_bf16 v[98:101], v[202:205], v[220:223], v[98:101]
	v_mfma_f32_16x16x32_bf16 v[86:89], v[194:197], v[228:231], v[86:89]
	v_mfma_f32_16x16x32_bf16 v[82:85], v[202:205], v[228:231], v[82:85]
	v_mfma_f32_16x16x32_bf16 v[70:73], v[194:197], v[236:239], v[70:73]
	v_mfma_f32_16x16x32_bf16 v[66:69], v[202:205], v[236:239], v[66:69]
	s_setprio 0
	s_barrier
	s_add_i32 s33, s59, s46
	v_lshl_add_u64 v[240:241], s[0:1], 0, v[132:133]
	s_mov_b32 m0, s33
	ds_read_b128 v[206:209], v176 offset:16384
	ds_read_b128 v[212:215], v176 offset:17408
	ds_read_b128 v[216:219], v176 offset:18432
	ds_read_b128 v[220:223], v176 offset:19456
	ds_read_b128 v[224:227], v176 offset:20480
	ds_read_b128 v[228:231], v176 offset:21504
	ds_read_b128 v[232:235], v176 offset:22528
	ds_read_b128 v[236:239], v176 offset:23552
	global_load_lds_dwordx4 v[240:241], off
	s_add_i32 m0, s33, 0x2000
	v_lshl_add_u64 v[242:243], s[0:1], 0, v[136:137]
	s_add_u32 s0, s0, s14
	s_addc_u32 s1, s1, s15
	s_add_i32 s33, s61, s46
	global_load_lds_dwordx4 v[242:243], off
	v_lshl_add_u64 v[244:245], s[0:1], 0, v[132:133]
	s_mov_b32 m0, s33
	v_lshl_add_u64 v[246:247], s[0:1], 0, v[136:137]
	global_load_lds_dwordx4 v[244:245], off
	s_add_i32 m0, s33, 0x2000
	v_lshl_add_u64 v[248:249], s[42:43], 0, v[130:131]
	global_load_lds_dwordx4 v[246:247], off
	v_lshl_add_u64 v[250:251], s[42:43], 0, v[134:135]
	s_waitcnt vmcnt(6)
	s_waitcnt lgkmcnt(0)
	s_barrier
; #define PG8_STAGE(bufoff, gbase, voff) do { _Pragma("unroll") for (int _i = 0; _i < 2; ++_i) \
;         __builtin_amdgcn_global_load_lds((const unsigned*)((const char*)(gbase) + (voff)[_i]), (PG8_LAS unsigned*)(lds + (bufoff) + ldsw + _i * 8192), 16, 0, 0); } while (0)
; #define PG8_LDA(dst, b, h) do { _Pragma("unroll") for (int m = 0; m < 4; ++m) { const bf16x8 f0_ = *(const PG8_LAS bf16x8*)(lds + PG8_SA(b, h) + aoff + m * 2048), f1_ = *(const PG8_LAS bf16x8*)(lds + PG8_SA(b, h) + aoff + m * 2048 + 1024); dst[m].set(f0_, f1_); } } while (0)
; #define PG8_LDB(dst, b, h) do { _Pragma("unroll") for (int n = 0; n < 2; ++n) { const bf16x8 f0_ = *(const PG8_LAS bf16x8*)(lds + PG8_SB(b, h) + boff + n * 2048), f1_ = *(const PG8_LAS bf16x8*)(lds + PG8_SB(b, h) + boff + n * 2048 + 1024); dst[n].set(f0_, f1_); } } while (0)
; #define PG8_WAIT_V(n) asm volatile("s_waitcnt vmcnt(" #n ")" ::: "memory")
; #define PG8_WAIT_L(n) asm volatile("s_waitcnt lgkmcnt(" #n ")" ::: "memory")
; #define PG8_BAR __builtin_amdgcn_s_barrier()
; #define PG8_SCHED __builtin_amdgcn_sched_barrier(0)
; template <class Epi, class Sched, bool ALIGN_EPI = false, bool SP2 = false>
; __device__ __forceinline__ void gemm_phase(PG8_LAS unsigned char* lds, const Gemm g, const Sched& S, const Epi& E) {
;     ...
;             PG8_WAIT_V(8); PG8_WAIT_L(0); PG8_BAR; PG8_MMA(1, 0, At, B0); PG8_MMA(1, 1, At, B1); PG8_BAR; PG8_SCHED;
;             PG8_LDB(B0, 1, 0); PG8_LDB(B1, 1, 1); PG8_SCHED; PG8_LDA(At, 1, 0); PG8_STAGE(PG8_SA(0, 1), a2 + hstep, voffA);
;             PG8_WAIT_V(8); PG8_WAIT_L(0); PG8_BAR; PG8_MMA(0, 0, At, B0); PG8_MMA(0, 1, At, B1); PG8_BAR; PG8_SCHED;
	s_setprio 1
	s_waitcnt lgkmcnt(0)
	v_mfma_f32_16x16x32_bf16 v[62:65], v[168:171], v[206:209], v[62:65]
	v_mfma_f32_16x16x32_bf16 v[58:61], v[182:185], v[206:209], v[58:61]
	v_mfma_f32_16x16x32_bf16 v[46:49], v[168:171], v[216:219], v[46:49]
	v_mfma_f32_16x16x32_bf16 v[42:45], v[182:185], v[216:219], v[42:45]
	v_mfma_f32_16x16x32_bf16 v[30:33], v[168:171], v[224:227], v[30:33]
	v_mfma_f32_16x16x32_bf16 v[26:29], v[182:185], v[224:227], v[26:29]
	v_mfma_f32_16x16x32_bf16 v[14:17], v[168:171], v[232:235], v[14:17]
	v_mfma_f32_16x16x32_bf16 v[10:13], v[182:185], v[232:235], v[10:13]
	v_mfma_f32_16x16x32_bf16 v[62:65], v[178:181], v[212:215], v[62:65]
	v_mfma_f32_16x16x32_bf16 v[58:61], v[186:189], v[212:215], v[58:61]
	v_mfma_f32_16x16x32_bf16 v[46:49], v[178:181], v[220:223], v[46:49]
	v_mfma_f32_16x16x32_bf16 v[42:45], v[186:189], v[220:223], v[42:45]
	v_mfma_f32_16x16x32_bf16 v[30:33], v[178:181], v[228:231], v[30:33]
	v_mfma_f32_16x16x32_bf16 v[26:29], v[186:189], v[228:231], v[26:29]
	v_mfma_f32_16x16x32_bf16 v[14:17], v[178:181], v[236:239], v[14:17]
	v_mfma_f32_16x16x32_bf16 v[10:13], v[186:189], v[236:239], v[10:13]
	s_setprio 0
	s_setprio 1
	v_mfma_f32_16x16x32_bf16 v[54:57], v[190:193], v[206:209], v[54:57]
	v_mfma_f32_16x16x32_bf16 v[50:53], v[198:201], v[206:209], v[50:53]
	v_mfma_f32_16x16x32_bf16 v[38:41], v[190:193], v[216:219], v[38:41]
	v_mfma_f32_16x16x32_bf16 v[34:37], v[198:201], v[216:219], v[34:37]
	v_mfma_f32_16x16x32_bf16 v[22:25], v[190:193], v[224:227], v[22:25]
	v_mfma_f32_16x16x32_bf16 v[18:21], v[198:201], v[224:227], v[18:21]
	v_mfma_f32_16x16x32_bf16 v[6:9], v[190:193], v[232:235], v[6:9]
	v_mfma_f32_16x16x32_bf16 v[2:5], v[198:201], v[232:235], v[2:5]
	v_mfma_f32_16x16x32_bf16 v[54:57], v[194:197], v[212:215], v[54:57]
	v_mfma_f32_16x16x32_bf16 v[50:53], v[202:205], v[212:215], v[50:53]
	v_mfma_f32_16x16x32_bf16 v[38:41], v[194:197], v[220:223], v[38:41]
	v_mfma_f32_16x16x32_bf16 v[34:37], v[202:205], v[220:223], v[34:37]
	v_mfma_f32_16x16x32_bf16 v[22:25], v[194:197], v[228:231], v[22:25]
	v_mfma_f32_16x16x32_bf16 v[18:21], v[202:205], v[228:231], v[18:21]
	v_mfma_f32_16x16x32_bf16 v[6:9], v[194:197], v[236:239], v[6:9]
	v_mfma_f32_16x16x32_bf16 v[2:5], v[202:205], v[236:239], v[2:5]
	s_setprio 0
	s_barrier
	s_add_i32 s33, 0, 0x18000
	s_add_i32 s76, 0, 0x1c000
	v_add_u32_e32 v186, s33, v173
	v_add_u32_e32 v202, s76, v173
	ds_read_b128 v[168:171], v186
	ds_read_b128 v[178:181], v186 offset:1024
	ds_read_b128 v[182:185], v186 offset:2048
	ds_read_b128 v[186:189], v186 offset:3072
	ds_read_b128 v[190:193], v202
	ds_read_b128 v[194:197], v202 offset:1024
	ds_read_b128 v[198:201], v202 offset:2048
	ds_read_b128 v[202:205], v202 offset:3072
	s_add_u32 s0, s42, s12
	s_addc_u32 s1, s43, s13
	s_mov_b32 m0, s49
	v_lshl_add_u64 v[252:253], s[0:1], 0, v[130:131]
	ds_read_b128 v[206:209], v176 offset:32768
	ds_read_b128 v[212:215], v176 offset:33792
	ds_read_b128 v[216:219], v176 offset:34816
	ds_read_b128 v[220:223], v176 offset:35840
	ds_read_b128 v[224:227], v176 offset:36864
	ds_read_b128 v[228:231], v176 offset:37888
	ds_read_b128 v[232:235], v176 offset:38912
	ds_read_b128 v[236:239], v176 offset:39936
	s_mov_b32 m0, s47
	s_nop 0
	global_load_lds_dwordx4 v[248:249], off
	s_mov_b32 m0, s48
	s_nop 0
	global_load_lds_dwordx4 v[250:251], off
	s_mov_b32 m0, s49
	s_nop 0
	global_load_lds_dwordx4 v[252:253], off
	v_lshl_add_u64 v[252:253], s[0:1], 0, v[134:135]
	s_mov_b32 m0, s50
	s_nop 0
	global_load_lds_dwordx4 v[252:253], off
	s_waitcnt vmcnt(8)
	s_waitcnt lgkmcnt(0)
	s_barrier
; #define PG8_STAGE(bufoff, gbase, voff) do { _Pragma("unroll") for (int _i = 0; _i < 2; ++_i) \
;         __builtin_amdgcn_global_load_lds((const unsigned*)((const char*)(gbase) + (voff)[_i]), (PG8_LAS unsigned*)(lds + (bufoff) + ldsw + _i * 8192), 16, 0, 0); } while (0)
; #define PG8_LDA(dst, b, h) do { _Pragma("unroll") for (int m = 0; m < 4; ++m) { const bf16x8 f0_ = *(const PG8_LAS bf16x8*)(lds + PG8_SA(b, h) + aoff + m * 2048), f1_ = *(const PG8_LAS bf16x8*)(lds + PG8_SA(b, h) + aoff + m * 2048 + 1024); dst[m].set(f0_, f1_); } } while (0)
; #define PG8_WAIT_V(n) asm volatile("s_waitcnt vmcnt(" #n ")" ::: "memory")
; #define PG8_WAIT_L(n) asm volatile("s_waitcnt lgkmcnt(" #n ")" ::: "memory")
; #define PG8_BAR __builtin_amdgcn_s_barrier()
; #define PG8_SCHED __builtin_amdgcn_sched_barrier(0)
; template <class Epi, class Sched, bool ALIGN_EPI = false, bool SP2 = false>
; __device__ __forceinline__ void gemm_phase(PG8_LAS unsigned char* lds, const Gemm g, const Sched& S, const Epi& E) {
;     ...
;             PG8_WAIT_V(8); PG8_WAIT_L(0); PG8_BAR; PG8_MMA(0, 0, At, B0); PG8_MMA(0, 1, At, B1); PG8_BAR; PG8_SCHED;
;             PG8_LDA(At, 1, 1); PG8_STAGE(PG8_SB(1, 0), b3, voffB); PG8_STAGE(PG8_SB(1, 1), b3 + hstepB, voffB); PG8_STAGE(PG8_SA(1, 0), a3, voffA);
;             PG8_WAIT_V(8); PG8_WAIT_L(0); PG8_BAR; PG8_MMA(1, 0, At, B0); PG8_MMA(1, 1, At, B1); PG8_BAR; PG8_SCHED;
	s_setprio 1
	s_waitcnt lgkmcnt(0)
	v_mfma_f32_16x16x32_bf16 v[126:129], v[168:171], v[206:209], v[126:129]
	v_mfma_f32_16x16x32_bf16 v[122:125], v[182:185], v[206:209], v[122:125]
	v_mfma_f32_16x16x32_bf16 v[110:113], v[168:171], v[216:219], v[110:113]
	v_mfma_f32_16x16x32_bf16 v[106:109], v[182:185], v[216:219], v[106:109]
	v_mfma_f32_16x16x32_bf16 v[94:97], v[168:171], v[224:227], v[94:97]
	v_mfma_f32_16x16x32_bf16 v[90:93], v[182:185], v[224:227], v[90:93]
	v_mfma_f32_16x16x32_bf16 v[78:81], v[168:171], v[232:235], v[78:81]
	v_mfma_f32_16x16x32_bf16 v[74:77], v[182:185], v[232:235], v[74:77]
	v_mfma_f32_16x16x32_bf16 v[126:129], v[178:181], v[212:215], v[126:129]
	v_mfma_f32_16x16x32_bf16 v[122:125], v[186:189], v[212:215], v[122:125]
	v_mfma_f32_16x16x32_bf16 v[110:113], v[178:181], v[220:223], v[110:113]
	v_mfma_f32_16x16x32_bf16 v[106:109], v[186:189], v[220:223], v[106:109]
	v_mfma_f32_16x16x32_bf16 v[94:97], v[178:181], v[228:231], v[94:97]
	v_mfma_f32_16x16x32_bf16 v[90:93], v[186:189], v[228:231], v[90:93]
	v_mfma_f32_16x16x32_bf16 v[78:81], v[178:181], v[236:239], v[78:81]
	v_mfma_f32_16x16x32_bf16 v[74:77], v[186:189], v[236:239], v[74:77]
	s_setprio 0
	s_setprio 1
	v_mfma_f32_16x16x32_bf16 v[118:121], v[190:193], v[206:209], v[118:121]
	v_mfma_f32_16x16x32_bf16 v[114:117], v[198:201], v[206:209], v[114:117]
	v_mfma_f32_16x16x32_bf16 v[102:105], v[190:193], v[216:219], v[102:105]
	v_mfma_f32_16x16x32_bf16 v[98:101], v[198:201], v[216:219], v[98:101]
	v_mfma_f32_16x16x32_bf16 v[86:89], v[190:193], v[224:227], v[86:89]
	v_mfma_f32_16x16x32_bf16 v[82:85], v[198:201], v[224:227], v[82:85]
	v_mfma_f32_16x16x32_bf16 v[70:73], v[190:193], v[232:235], v[70:73]
	v_mfma_f32_16x16x32_bf16 v[66:69], v[198:201], v[232:235], v[66:69]
	v_mfma_f32_16x16x32_bf16 v[118:121], v[194:197], v[212:215], v[118:121]
	v_mfma_f32_16x16x32_bf16 v[114:117], v[202:205], v[212:215], v[114:117]
	v_mfma_f32_16x16x32_bf16 v[102:105], v[194:197], v[220:223], v[102:105]
	v_mfma_f32_16x16x32_bf16 v[98:101], v[202:205], v[220:223], v[98:101]
	v_mfma_f32_16x16x32_bf16 v[86:89], v[194:197], v[228:231], v[86:89]
	v_mfma_f32_16x16x32_bf16 v[82:85], v[202:205], v[228:231], v[82:85]
	v_mfma_f32_16x16x32_bf16 v[70:73], v[194:197], v[236:239], v[70:73]
	v_mfma_f32_16x16x32_bf16 v[66:69], v[202:205], v[236:239], v[66:69]
	s_setprio 0
	s_barrier
	s_add_i32 s0, s33, s46
	v_lshl_add_u64 v[240:241], v[240:241], 0, s[26:27]
	s_mov_b32 m0, s0
	ds_read_b128 v[206:209], v176 offset:49152
	ds_read_b128 v[212:215], v176 offset:50176
	ds_read_b128 v[216:219], v176 offset:51200
	ds_read_b128 v[220:223], v176 offset:52224
	ds_read_b128 v[224:227], v176 offset:53248
	ds_read_b128 v[228:231], v176 offset:54272
	ds_read_b128 v[232:235], v176 offset:55296
	ds_read_b128 v[236:239], v176 offset:56320
	global_load_lds_dwordx4 v[240:241], off
	v_lshl_add_u64 v[240:241], v[242:243], 0, s[26:27]
	s_add_i32 m0, s0, 0x2000
	s_add_i32 s0, s76, s46
	global_load_lds_dwordx4 v[240:241], off
	v_lshl_add_u64 v[240:241], v[244:245], 0, s[26:27]
	s_mov_b32 m0, s0
	s_nop 0
	global_load_lds_dwordx4 v[240:241], off
	v_lshl_add_u64 v[240:241], v[246:247], 0, s[26:27]
	s_add_i32 m0, s0, 0x2000
	s_nop 0
	global_load_lds_dwordx4 v[240:241], off
	v_lshl_add_u64 v[240:241], v[248:249], 0, s[26:27]
	s_mov_b32 m0, s52
	s_nop 0
	global_load_lds_dwordx4 v[240:241], off
	v_lshl_add_u64 v[240:241], v[250:251], 0, s[26:27]
	s_mov_b32 m0, s53
	s_nop 0
	global_load_lds_dwordx4 v[240:241], off
	s_waitcnt vmcnt(6)
	s_waitcnt lgkmcnt(0)
	s_barrier
	s_setprio 1
	s_waitcnt lgkmcnt(0)
	v_mfma_f32_16x16x32_bf16 v[62:65], v[168:171], v[206:209], v[62:65]
	v_mfma_f32_16x16x32_bf16 v[58:61], v[182:185], v[206:209], v[58:61]
	v_mfma_f32_16x16x32_bf16 v[46:49], v[168:171], v[216:219], v[46:49]
	v_mfma_f32_16x16x32_bf16 v[42:45], v[182:185], v[216:219], v[42:45]
	v_mfma_f32_16x16x32_bf16 v[30:33], v[168:171], v[224:227], v[30:33]
	v_mfma_f32_16x16x32_bf16 v[26:29], v[182:185], v[224:227], v[26:29]
	v_mfma_f32_16x16x32_bf16 v[14:17], v[168:171], v[232:235], v[14:17]
	v_mfma_f32_16x16x32_bf16 v[10:13], v[182:185], v[232:235], v[10:13]
	v_mfma_f32_16x16x32_bf16 v[62:65], v[178:181], v[212:215], v[62:65]
	v_mfma_f32_16x16x32_bf16 v[58:61], v[186:189], v[212:215], v[58:61]
	v_mfma_f32_16x16x32_bf16 v[46:49], v[178:181], v[220:223], v[46:49]
	v_mfma_f32_16x16x32_bf16 v[42:45], v[186:189], v[220:223], v[42:45]
	v_mfma_f32_16x16x32_bf16 v[30:33], v[178:181], v[228:231], v[30:33]
	v_mfma_f32_16x16x32_bf16 v[26:29], v[186:189], v[228:231], v[26:29]
	v_mfma_f32_16x16x32_bf16 v[14:17], v[178:181], v[236:239], v[14:17]
	v_mfma_f32_16x16x32_bf16 v[10:13], v[186:189], v[236:239], v[10:13]
	s_setprio 0
	s_setprio 1
	v_mfma_f32_16x16x32_bf16 v[54:57], v[190:193], v[206:209], v[54:57]
	v_mfma_f32_16x16x32_bf16 v[50:53], v[198:201], v[206:209], v[50:53]
	v_mfma_f32_16x16x32_bf16 v[38:41], v[190:193], v[216:219], v[38:41]
	v_mfma_f32_16x16x32_bf16 v[34:37], v[198:201], v[216:219], v[34:37]
	v_mfma_f32_16x16x32_bf16 v[22:25], v[190:193], v[224:227], v[22:25]
	v_mfma_f32_16x16x32_bf16 v[18:21], v[198:201], v[224:227], v[18:21]
	v_mfma_f32_16x16x32_bf16 v[6:9], v[190:193], v[232:235], v[6:9]
	v_mfma_f32_16x16x32_bf16 v[2:5], v[198:201], v[232:235], v[2:5]
	v_mfma_f32_16x16x32_bf16 v[54:57], v[194:197], v[212:215], v[54:57]
	v_mfma_f32_16x16x32_bf16 v[50:53], v[202:205], v[212:215], v[50:53]
	v_mfma_f32_16x16x32_bf16 v[38:41], v[194:197], v[220:223], v[38:41]
	v_mfma_f32_16x16x32_bf16 v[34:37], v[202:205], v[220:223], v[34:37]
	v_mfma_f32_16x16x32_bf16 v[22:25], v[194:197], v[228:231], v[22:25]
	v_mfma_f32_16x16x32_bf16 v[18:21], v[202:205], v[228:231], v[18:21]
	v_mfma_f32_16x16x32_bf16 v[6:9], v[194:197], v[236:239], v[6:9]
	v_mfma_f32_16x16x32_bf16 v[2:5], v[202:205], v[236:239], v[2:5]
	s_setprio 0
	s_barrier
	s_add_u32 s40, s40, 0x100
	s_addc_u32 s41, s41, 0
	s_cmp_ge_i32 s75, s54
	s_cbranch_scc0 .LBB0_982

; #define PG8_STAGE(bufoff, gbase, voff) do { _Pragma("unroll") for (int _i = 0; _i < 2; ++_i) \
;         __builtin_amdgcn_global_load_lds((const unsigned*)((const char*)(gbase) + (voff)[_i]), (PG8_LAS unsigned*)(lds + (bufoff) + ldsw + _i * 8192), 16, 0, 0); } while (0)
; #define PG8_LDA(dst, b, h) do { _Pragma("unroll") for (int m = 0; m < 4; ++m) { const bf16x8 f0_ = *(const PG8_LAS bf16x8*)(lds + PG8_SA(b, h) + aoff + m * 2048), f1_ = *(const PG8_LAS bf16x8*)(lds + PG8_SA(b, h) + aoff + m * 2048 + 1024); dst[m].set(f0_, f1_); } } while (0)
; #define PG8_LDB(dst, b, h) do { _Pragma("unroll") for (int n = 0; n < 2; ++n) { const bf16x8 f0_ = *(const PG8_LAS bf16x8*)(lds + PG8_SB(b, h) + boff + n * 2048), f1_ = *(const PG8_LAS bf16x8*)(lds + PG8_SB(b, h) + boff + n * 2048 + 1024); dst[n].set(f0_, f1_); } } while (0)
; #define PG8_WAIT_V(n) asm volatile("s_waitcnt vmcnt(" #n ")" ::: "memory")
; #define PG8_WAIT_L(n) asm volatile("s_waitcnt lgkmcnt(" #n ")" ::: "memory")
; #define PG8_BAR __builtin_amdgcn_s_barrier()
; #define PG8_SCHED __builtin_amdgcn_sched_barrier(0)
; template <class Epi, class Sched, bool ALIGN_EPI = false, bool SP2 = false>
; __device__ __forceinline__ void gemm_phase(PG8_LAS unsigned char* lds, const Gemm g, const Sched& S, const Epi& E) {
;     ...
;             const bool last = (t == nt - 2);
;             const char* a1 = cA + (size_t)(t + 1) * kstep;
;             const char* a2 = last ? nA : cA + (size_t)(t + 2) * kstep; const char* b2 = last ? nB : cB + (size_t)(t + 2) * kstep;
;             const char* a3 = a2 + kstep; const char* b3 = b2 + kstep;
;             if (last && has_next) S.a_ready(nxt);
;             if constexpr (SP2) {
;             PG8_LDB(B0, 0, 0); PG8_LDB(B1, 0, 1); PG8_SCHED; PG8_LDA(At, 0, 0); PG8_STAGE(PG8_SA(1, 1), a1 + hstep, voffA);
;             PG8_WAIT_V(8); PG8_WAIT_L(0); PG8_BAR; PG8_MMA(0, 0, At, B0); PG8_MMA(0, 1, At, B1); PG8_BAR; PG8_SCHED;
;             PG8_LDA(At, 0, 1); PG8_STAGE(PG8_SB(0, 0), b2, voffB); PG8_STAGE(PG8_SB(0, 1), b2 + hstepB, voffB); PG8_STAGE(PG8_SA(0, 0), a2, voffA);
;             PG8_WAIT_V(8); PG8_WAIT_L(0); PG8_BAR; PG8_MMA(1, 0, At, B0); PG8_MMA(1, 1, At, B1); PG8_BAR; PG8_SCHED;
.LBB0_1070:
	ds_read_b128 v[130:133], v193
	ds_read_b128 v[134:137], v193 offset:1024
	ds_read_b128 v[138:141], v193 offset:2048
	ds_read_b128 v[142:145], v193 offset:3072
	ds_read_b128 v[146:149], v194
	ds_read_b128 v[150:153], v194 offset:1024
	ds_read_b128 v[154:157], v194 offset:2048
	ds_read_b128 v[158:161], v194 offset:3072
	s_add_i32 s95, s58, 2
	s_add_u32 s0, s56, 0x80
	s_addc_u32 s1, s57, 0
	s_cmp_eq_u32 s78, s58
	s_cselect_b32 s58, s2, s0
	s_cselect_b32 s59, s3, s1
	s_cselect_b32 s1, s55, s94
	s_cselect_b32 s0, s54, s93
	s_cmp_eq_u32 s99, 0
	s_cbranch_scc1 .Lkr2_a
	v_lshl_add_u64 v[232:233], v[232:233], 0, s[28:29]
	s_mov_b32 m0, s74
	v_lshl_add_u64 v[234:235], v[234:235], 0, s[28:29]
	global_load_lds_dwordx4 v[232:233], off
	s_mov_b32 m0, s75
	s_nop 0
	global_load_lds_dwordx4 v[234:235], off
.Lkr2_a:
	v_lshl_add_u64 v[224:225], s[56:57], 0, v[176:177]
	s_add_i32 m0, s67, 0xc000
	ds_read_b128 v[162:165], v195
	ds_read_b128 v[186:189], v195 offset:1024
	ds_read_b128 v[198:201], v195 offset:2048
	ds_read_b128 v[202:205], v195 offset:3072
	ds_read_b128 v[206:209], v195 offset:4096
	ds_read_b128 v[212:215], v195 offset:5120
	ds_read_b128 v[216:219], v195 offset:6144
	ds_read_b128 v[220:223], v195 offset:7168
	global_load_lds_dwordx4 v[224:225], off
	v_lshl_add_u64 v[224:225], s[56:57], 0, v[178:179]
	s_add_i32 m0, s67, 0xe000
	s_nop 0
	global_load_lds_dwordx4 v[224:225], off
	s_waitcnt vmcnt(8)
	s_waitcnt lgkmcnt(0)
	s_barrier
	s_setprio 1
	s_waitcnt lgkmcnt(0)
	v_mfma_f32_16x16x32_bf16 v[126:129], v[130:133], v[162:165], v[126:129]
	v_mfma_f32_16x16x32_bf16 v[122:125], v[138:141], v[162:165], v[122:125]
	v_mfma_f32_16x16x32_bf16 v[58:61], v[130:133], v[198:201], v[58:61]
	v_mfma_f32_16x16x32_bf16 v[62:65], v[138:141], v[198:201], v[62:65]
	v_mfma_f32_16x16x32_bf16 v[106:109], v[130:133], v[206:209], v[106:109]
	v_mfma_f32_16x16x32_bf16 v[110:113], v[138:141], v[206:209], v[110:113]
	v_mfma_f32_16x16x32_bf16 v[98:101], v[130:133], v[216:219], v[98:101]
	v_mfma_f32_16x16x32_bf16 v[102:105], v[138:141], v[216:219], v[102:105]
	v_mfma_f32_16x16x32_bf16 v[126:129], v[134:137], v[186:189], v[126:129]
	v_mfma_f32_16x16x32_bf16 v[122:125], v[142:145], v[186:189], v[122:125]
	v_mfma_f32_16x16x32_bf16 v[58:61], v[134:137], v[202:205], v[58:61]
	v_mfma_f32_16x16x32_bf16 v[62:65], v[142:145], v[202:205], v[62:65]
	v_mfma_f32_16x16x32_bf16 v[106:109], v[134:137], v[212:215], v[106:109]
	v_mfma_f32_16x16x32_bf16 v[110:113], v[142:145], v[212:215], v[110:113]
	v_mfma_f32_16x16x32_bf16 v[98:101], v[134:137], v[220:223], v[98:101]
	v_mfma_f32_16x16x32_bf16 v[102:105], v[142:145], v[220:223], v[102:105]
	s_setprio 0
	s_setprio 1
	v_mfma_f32_16x16x32_bf16 v[118:121], v[146:149], v[162:165], v[118:121]
	v_mfma_f32_16x16x32_bf16 v[114:117], v[154:157], v[162:165], v[114:117]
	v_mfma_f32_16x16x32_bf16 v[50:53], v[146:149], v[198:201], v[50:53]
	v_mfma_f32_16x16x32_bf16 v[54:57], v[154:157], v[198:201], v[54:57]
	v_mfma_f32_16x16x32_bf16 v[90:93], v[146:149], v[206:209], v[90:93]
	v_mfma_f32_16x16x32_bf16 v[94:97], v[154:157], v[206:209], v[94:97]
	v_mfma_f32_16x16x32_bf16 v[74:77], v[146:149], v[216:219], v[74:77]
	v_mfma_f32_16x16x32_bf16 v[78:81], v[154:157], v[216:219], v[78:81]
	v_mfma_f32_16x16x32_bf16 v[118:121], v[150:153], v[186:189], v[118:121]
	v_mfma_f32_16x16x32_bf16 v[114:117], v[158:161], v[186:189], v[114:117]
	v_mfma_f32_16x16x32_bf16 v[50:53], v[150:153], v[202:205], v[50:53]
	v_mfma_f32_16x16x32_bf16 v[54:57], v[158:161], v[202:205], v[54:57]
	v_mfma_f32_16x16x32_bf16 v[90:93], v[150:153], v[212:215], v[90:93]
	v_mfma_f32_16x16x32_bf16 v[94:97], v[158:161], v[212:215], v[94:97]
	v_mfma_f32_16x16x32_bf16 v[74:77], v[150:153], v[220:223], v[74:77]
	v_mfma_f32_16x16x32_bf16 v[78:81], v[158:161], v[220:223], v[78:81]
	s_setprio 0
	s_barrier
	s_add_i32 s33, s82, s66
	v_lshl_add_u64 v[224:225], s[0:1], 0, v[168:169]
	s_mov_b32 m0, s33
	ds_read_b128 v[162:165], v195 offset:16384
	ds_read_b128 v[186:189], v195 offset:17408
	ds_read_b128 v[198:201], v195 offset:18432
	ds_read_b128 v[202:205], v195 offset:19456
	ds_read_b128 v[206:209], v195 offset:20480
	ds_read_b128 v[212:215], v195 offset:21504
	ds_read_b128 v[216:219], v195 offset:22528
	ds_read_b128 v[220:223], v195 offset:23552
	global_load_lds_dwordx4 v[224:225], off
	s_add_i32 m0, s33, 0x2000
	v_lshl_add_u64 v[226:227], s[0:1], 0, v[172:173]
	s_add_u32 s0, s0, s16
	s_addc_u32 s1, s1, s17
	s_add_i32 s33, s83, s66
	global_load_lds_dwordx4 v[226:227], off
	v_lshl_add_u64 v[228:229], s[0:1], 0, v[168:169]
	s_mov_b32 m0, s33
	v_lshl_add_u64 v[230:231], s[0:1], 0, v[172:173]
	global_load_lds_dwordx4 v[228:229], off
	s_add_i32 m0, s33, 0x2000
	v_lshl_add_u64 v[232:233], s[58:59], 0, v[166:167]
	global_load_lds_dwordx4 v[230:231], off
	v_lshl_add_u64 v[234:235], s[58:59], 0, v[170:171]
	s_waitcnt vmcnt(6)
	s_waitcnt lgkmcnt(0)
	s_barrier
; #define PG8_STAGE(bufoff, gbase, voff) do { _Pragma("unroll") for (int _i = 0; _i < 2; ++_i) \
;         __builtin_amdgcn_global_load_lds((const unsigned*)((const char*)(gbase) + (voff)[_i]), (PG8_LAS unsigned*)(lds + (bufoff) + ldsw + _i * 8192), 16, 0, 0); } while (0)
; #define PG8_LDA(dst, b, h) do { _Pragma("unroll") for (int m = 0; m < 4; ++m) { const bf16x8 f0_ = *(const PG8_LAS bf16x8*)(lds + PG8_SA(b, h) + aoff + m * 2048), f1_ = *(const PG8_LAS bf16x8*)(lds + PG8_SA(b, h) + aoff + m * 2048 + 1024); dst[m].set(f0_, f1_); } } while (0)
; #define PG8_LDB(dst, b, h) do { _Pragma("unroll") for (int n = 0; n < 2; ++n) { const bf16x8 f0_ = *(const PG8_LAS bf16x8*)(lds + PG8_SB(b, h) + boff + n * 2048), f1_ = *(const PG8_LAS bf16x8*)(lds + PG8_SB(b, h) + boff + n * 2048 + 1024); dst[n].set(f0_, f1_); } } while (0)
; #define PG8_WAIT_V(n) asm volatile("s_waitcnt vmcnt(" #n ")" ::: "memory")
; #define PG8_WAIT_L(n) asm volatile("s_waitcnt lgkmcnt(" #n ")" ::: "memory")
; #define PG8_BAR __builtin_amdgcn_s_barrier()
; #define PG8_SCHED __builtin_amdgcn_sched_barrier(0)
; template <class Epi, class Sched, bool ALIGN_EPI = false, bool SP2 = false>
; __device__ __forceinline__ void gemm_phase(PG8_LAS unsigned char* lds, const Gemm g, const Sched& S, const Epi& E) {
;     ...
;             PG8_WAIT_V(8); PG8_WAIT_L(0); PG8_BAR; PG8_MMA(1, 0, At, B0); PG8_MMA(1, 1, At, B1); PG8_BAR; PG8_SCHED;
;             PG8_LDB(B0, 1, 0); PG8_LDB(B1, 1, 1); PG8_SCHED; PG8_LDA(At, 1, 0); PG8_STAGE(PG8_SA(0, 1), a2 + hstep, voffA);
;             PG8_WAIT_V(8); PG8_WAIT_L(0); PG8_BAR; PG8_MMA(0, 0, At, B0); PG8_MMA(0, 1, At, B1); PG8_BAR; PG8_SCHED;
	s_setprio 1
	s_waitcnt lgkmcnt(0)
	v_mfma_f32_16x16x32_bf16 v[82:85], v[130:133], v[162:165], v[82:85]
	v_mfma_f32_16x16x32_bf16 v[86:89], v[138:141], v[162:165], v[86:89]
	v_mfma_f32_16x16x32_bf16 v[46:49], v[130:133], v[198:201], v[46:49]
	v_mfma_f32_16x16x32_bf16 v[42:45], v[138:141], v[198:201], v[42:45]
	v_mfma_f32_16x16x32_bf16 v[30:33], v[130:133], v[206:209], v[30:33]
	v_mfma_f32_16x16x32_bf16 v[26:29], v[138:141], v[206:209], v[26:29]
	v_mfma_f32_16x16x32_bf16 v[14:17], v[130:133], v[216:219], v[14:17]
	v_mfma_f32_16x16x32_bf16 v[6:9], v[138:141], v[216:219], v[6:9]
	v_mfma_f32_16x16x32_bf16 v[82:85], v[134:137], v[186:189], v[82:85]
	v_mfma_f32_16x16x32_bf16 v[86:89], v[142:145], v[186:189], v[86:89]
	v_mfma_f32_16x16x32_bf16 v[46:49], v[134:137], v[202:205], v[46:49]
	v_mfma_f32_16x16x32_bf16 v[42:45], v[142:145], v[202:205], v[42:45]
	v_mfma_f32_16x16x32_bf16 v[30:33], v[134:137], v[212:215], v[30:33]
	v_mfma_f32_16x16x32_bf16 v[26:29], v[142:145], v[212:215], v[26:29]
	v_mfma_f32_16x16x32_bf16 v[14:17], v[134:137], v[220:223], v[14:17]
	v_mfma_f32_16x16x32_bf16 v[6:9], v[142:145], v[220:223], v[6:9]
	s_setprio 0
	s_setprio 1
	v_mfma_f32_16x16x32_bf16 v[66:69], v[146:149], v[162:165], v[66:69]
	v_mfma_f32_16x16x32_bf16 v[70:73], v[154:157], v[162:165], v[70:73]
	v_mfma_f32_16x16x32_bf16 v[38:41], v[146:149], v[198:201], v[38:41]
	v_mfma_f32_16x16x32_bf16 v[34:37], v[154:157], v[198:201], v[34:37]
	v_mfma_f32_16x16x32_bf16 v[22:25], v[146:149], v[206:209], v[22:25]
	v_mfma_f32_16x16x32_bf16 v[18:21], v[154:157], v[206:209], v[18:21]
	v_mfma_f32_16x16x32_bf16 v[10:13], v[146:149], v[216:219], v[10:13]
	v_mfma_f32_16x16x32_bf16 v[2:5], v[154:157], v[216:219], v[2:5]
	v_mfma_f32_16x16x32_bf16 v[66:69], v[150:153], v[186:189], v[66:69]
	v_mfma_f32_16x16x32_bf16 v[70:73], v[158:161], v[186:189], v[70:73]
	v_mfma_f32_16x16x32_bf16 v[38:41], v[150:153], v[202:205], v[38:41]
	v_mfma_f32_16x16x32_bf16 v[34:37], v[158:161], v[202:205], v[34:37]
	v_mfma_f32_16x16x32_bf16 v[22:25], v[150:153], v[212:215], v[22:25]
	v_mfma_f32_16x16x32_bf16 v[18:21], v[158:161], v[212:215], v[18:21]
	v_mfma_f32_16x16x32_bf16 v[10:13], v[150:153], v[220:223], v[10:13]
	v_mfma_f32_16x16x32_bf16 v[2:5], v[158:161], v[220:223], v[2:5]
	s_setprio 0
	s_barrier
	s_add_i32 s33, 0, 0x18000
	s_add_i32 s96, 0, 0x1c000
	v_add_u32_e32 v142, s33, v190
	v_add_u32_e32 v158, s96, v190
	ds_read_b128 v[130:133], v142
	ds_read_b128 v[134:137], v142 offset:1024
	ds_read_b128 v[138:141], v142 offset:2048
	ds_read_b128 v[142:145], v142 offset:3072
	ds_read_b128 v[146:149], v158
	ds_read_b128 v[150:153], v158 offset:1024
	ds_read_b128 v[154:157], v158 offset:2048
	ds_read_b128 v[158:161], v158 offset:3072
	s_add_u32 s0, s58, s14
	s_addc_u32 s1, s59, s15
	s_mov_b32 m0, s71
	v_lshl_add_u64 v[236:237], s[0:1], 0, v[166:167]
	ds_read_b128 v[162:165], v195 offset:32768
	ds_read_b128 v[186:189], v195 offset:33792
	ds_read_b128 v[198:201], v195 offset:34816
	ds_read_b128 v[202:205], v195 offset:35840
	ds_read_b128 v[206:209], v195 offset:36864
	ds_read_b128 v[212:215], v195 offset:37888
	ds_read_b128 v[216:219], v195 offset:38912
	ds_read_b128 v[220:223], v195 offset:39936
	s_mov_b32 m0, s67
	s_nop 0
	global_load_lds_dwordx4 v[232:233], off
	s_mov_b32 m0, s69
	s_nop 0
	global_load_lds_dwordx4 v[234:235], off
	s_mov_b32 m0, s71
	s_nop 0
	global_load_lds_dwordx4 v[236:237], off
	v_lshl_add_u64 v[236:237], s[0:1], 0, v[170:171]
	s_mov_b32 m0, s73
	s_nop 0
	global_load_lds_dwordx4 v[236:237], off
	s_waitcnt vmcnt(8)
	s_waitcnt lgkmcnt(0)
	s_barrier
	s_setprio 1
	s_waitcnt lgkmcnt(0)
	v_mfma_f32_16x16x32_bf16 v[126:129], v[130:133], v[162:165], v[126:129]
	v_mfma_f32_16x16x32_bf16 v[122:125], v[138:141], v[162:165], v[122:125]
	v_mfma_f32_16x16x32_bf16 v[58:61], v[130:133], v[198:201], v[58:61]
	v_mfma_f32_16x16x32_bf16 v[62:65], v[138:141], v[198:201], v[62:65]
	v_mfma_f32_16x16x32_bf16 v[106:109], v[130:133], v[206:209], v[106:109]
	v_mfma_f32_16x16x32_bf16 v[110:113], v[138:141], v[206:209], v[110:113]
	v_mfma_f32_16x16x32_bf16 v[98:101], v[130:133], v[216:219], v[98:101]
	v_mfma_f32_16x16x32_bf16 v[102:105], v[138:141], v[216:219], v[102:105]
	v_mfma_f32_16x16x32_bf16 v[126:129], v[134:137], v[186:189], v[126:129]
	v_mfma_f32_16x16x32_bf16 v[122:125], v[142:145], v[186:189], v[122:125]
	v_mfma_f32_16x16x32_bf16 v[58:61], v[134:137], v[202:205], v[58:61]
	v_mfma_f32_16x16x32_bf16 v[62:65], v[142:145], v[202:205], v[62:65]
	v_mfma_f32_16x16x32_bf16 v[106:109], v[134:137], v[212:215], v[106:109]
	v_mfma_f32_16x16x32_bf16 v[110:113], v[142:145], v[212:215], v[110:113]
	v_mfma_f32_16x16x32_bf16 v[98:101], v[134:137], v[220:223], v[98:101]
	v_mfma_f32_16x16x32_bf16 v[102:105], v[142:145], v[220:223], v[102:105]
	s_setprio 0
	s_setprio 1
	v_mfma_f32_16x16x32_bf16 v[118:121], v[146:149], v[162:165], v[118:121]
	v_mfma_f32_16x16x32_bf16 v[114:117], v[154:157], v[162:165], v[114:117]
	v_mfma_f32_16x16x32_bf16 v[50:53], v[146:149], v[198:201], v[50:53]
	v_mfma_f32_16x16x32_bf16 v[54:57], v[154:157], v[198:201], v[54:57]
	v_mfma_f32_16x16x32_bf16 v[90:93], v[146:149], v[206:209], v[90:93]
	v_mfma_f32_16x16x32_bf16 v[94:97], v[154:157], v[206:209], v[94:97]
	v_mfma_f32_16x16x32_bf16 v[74:77], v[146:149], v[216:219], v[74:77]
	v_mfma_f32_16x16x32_bf16 v[78:81], v[154:157], v[216:219], v[78:81]
	v_mfma_f32_16x16x32_bf16 v[118:121], v[150:153], v[186:189], v[118:121]
	v_mfma_f32_16x16x32_bf16 v[114:117], v[158:161], v[186:189], v[114:117]
	v_mfma_f32_16x16x32_bf16 v[50:53], v[150:153], v[202:205], v[50:53]
	v_mfma_f32_16x16x32_bf16 v[54:57], v[158:161], v[202:205], v[54:57]
	v_mfma_f32_16x16x32_bf16 v[90:93], v[150:153], v[212:215], v[90:93]
	v_mfma_f32_16x16x32_bf16 v[94:97], v[158:161], v[212:215], v[94:97]
	v_mfma_f32_16x16x32_bf16 v[74:77], v[150:153], v[220:223], v[74:77]
	v_mfma_f32_16x16x32_bf16 v[78:81], v[158:161], v[220:223], v[78:81]
	s_setprio 0
	s_barrier
; #define PG8_STAGE(bufoff, gbase, voff) do { _Pragma("unroll") for (int _i = 0; _i < 2; ++_i) \
;         __builtin_amdgcn_global_load_lds((const unsigned*)((const char*)(gbase) + (voff)[_i]), (PG8_LAS unsigned*)(lds + (bufoff) + ldsw + _i * 8192), 16, 0, 0); } while (0)
; #define PG8_LDA(dst, b, h) do { _Pragma("unroll") for (int m = 0; m < 4; ++m) { const bf16x8 f0_ = *(const PG8_LAS bf16x8*)(lds + PG8_SA(b, h) + aoff + m * 2048), f1_ = *(const PG8_LAS bf16x8*)(lds + PG8_SA(b, h) + aoff + m * 2048 + 1024); dst[m].set(f0_, f1_); } } while (0)
; #define PG8_WAIT_V(n) asm volatile("s_waitcnt vmcnt(" #n ")" ::: "memory")
; #define PG8_WAIT_L(n) asm volatile("s_waitcnt lgkmcnt(" #n ")" ::: "memory")
; #define PG8_BAR __builtin_amdgcn_s_barrier()
; #define PG8_SCHED __builtin_amdgcn_sched_barrier(0)
; template <class Epi, class Sched, bool ALIGN_EPI = false, bool SP2 = false>
; __device__ __forceinline__ void gemm_phase(PG8_LAS unsigned char* lds, const Gemm g, const Sched& S, const Epi& E) {
;     ...
;             PG8_LDA(At, 1, 1); PG8_STAGE(PG8_SB(1, 0), b3, voffB); PG8_STAGE(PG8_SB(1, 1), b3 + hstepB, voffB); PG8_STAGE(PG8_SA(1, 0), a3, voffA);
;             PG8_WAIT_V(8); PG8_WAIT_L(0); PG8_BAR; PG8_MMA(1, 0, At, B0); PG8_MMA(1, 1, At, B1); PG8_BAR; PG8_SCHED;
	s_add_i32 s0, s33, s66
	v_lshl_add_u64 v[224:225], v[224:225], 0, s[28:29]
	s_mov_b32 m0, s0
	ds_read_b128 v[162:165], v195 offset:49152
	ds_read_b128 v[186:189], v195 offset:50176
	ds_read_b128 v[198:201], v195 offset:51200
	ds_read_b128 v[202:205], v195 offset:52224
	ds_read_b128 v[206:209], v195 offset:53248
	ds_read_b128 v[212:215], v195 offset:54272
	ds_read_b128 v[216:219], v195 offset:55296
	ds_read_b128 v[220:223], v195 offset:56320
	global_load_lds_dwordx4 v[224:225], off
	v_lshl_add_u64 v[224:225], v[226:227], 0, s[28:29]
	s_add_i32 m0, s0, 0x2000
	s_add_i32 s0, s96, s66
	global_load_lds_dwordx4 v[224:225], off
	v_lshl_add_u64 v[224:225], v[228:229], 0, s[28:29]
	s_mov_b32 m0, s0
	s_nop 0
	global_load_lds_dwordx4 v[224:225], off
	v_lshl_add_u64 v[224:225], v[230:231], 0, s[28:29]
	s_add_i32 m0, s0, 0x2000
	s_nop 0
	global_load_lds_dwordx4 v[224:225], off
	s_cmp_ge_i32 s95, s76
	s_cbranch_scc0 .Lkr2_b
	v_lshl_add_u64 v[224:225], v[232:233], 0, s[28:29]
	s_mov_b32 m0, s74
	s_nop 0
	global_load_lds_dwordx4 v[224:225], off
	v_lshl_add_u64 v[224:225], v[234:235], 0, s[28:29]
	s_mov_b32 m0, s75
	s_nop 0
	global_load_lds_dwordx4 v[224:225], off
.Lkr2_b:
	s_waitcnt vmcnt(6)
	s_waitcnt lgkmcnt(0)
	s_barrier
	s_setprio 1
	s_waitcnt lgkmcnt(0)
	v_mfma_f32_16x16x32_bf16 v[82:85], v[130:133], v[162:165], v[82:85]
	v_mfma_f32_16x16x32_bf16 v[86:89], v[138:141], v[162:165], v[86:89]
	v_mfma_f32_16x16x32_bf16 v[46:49], v[130:133], v[198:201], v[46:49]
	v_mfma_f32_16x16x32_bf16 v[42:45], v[138:141], v[198:201], v[42:45]
	v_mfma_f32_16x16x32_bf16 v[30:33], v[130:133], v[206:209], v[30:33]
	v_mfma_f32_16x16x32_bf16 v[26:29], v[138:141], v[206:209], v[26:29]
	v_mfma_f32_16x16x32_bf16 v[14:17], v[130:133], v[216:219], v[14:17]
	v_mfma_f32_16x16x32_bf16 v[6:9], v[138:141], v[216:219], v[6:9]
	v_mfma_f32_16x16x32_bf16 v[82:85], v[134:137], v[186:189], v[82:85]
	v_mfma_f32_16x16x32_bf16 v[86:89], v[142:145], v[186:189], v[86:89]
	v_mfma_f32_16x16x32_bf16 v[46:49], v[134:137], v[202:205], v[46:49]
	v_mfma_f32_16x16x32_bf16 v[42:45], v[142:145], v[202:205], v[42:45]
	v_mfma_f32_16x16x32_bf16 v[30:33], v[134:137], v[212:215], v[30:33]
	v_mfma_f32_16x16x32_bf16 v[26:29], v[142:145], v[212:215], v[26:29]
	v_mfma_f32_16x16x32_bf16 v[14:17], v[134:137], v[220:223], v[14:17]
	v_mfma_f32_16x16x32_bf16 v[6:9], v[142:145], v[220:223], v[6:9]
	s_setprio 0
	s_setprio 1
	v_mfma_f32_16x16x32_bf16 v[66:69], v[146:149], v[162:165], v[66:69]
	v_mfma_f32_16x16x32_bf16 v[70:73], v[154:157], v[162:165], v[70:73]
	v_mfma_f32_16x16x32_bf16 v[38:41], v[146:149], v[198:201], v[38:41]
	v_mfma_f32_16x16x32_bf16 v[34:37], v[154:157], v[198:201], v[34:37]
	v_mfma_f32_16x16x32_bf16 v[22:25], v[146:149], v[206:209], v[22:25]
	v_mfma_f32_16x16x32_bf16 v[18:21], v[154:157], v[206:209], v[18:21]
	v_mfma_f32_16x16x32_bf16 v[10:13], v[146:149], v[216:219], v[10:13]
	v_mfma_f32_16x16x32_bf16 v[2:5], v[154:157], v[216:219], v[2:5]
	v_mfma_f32_16x16x32_bf16 v[66:69], v[150:153], v[186:189], v[66:69]
	v_mfma_f32_16x16x32_bf16 v[70:73], v[158:161], v[186:189], v[70:73]
	v_mfma_f32_16x16x32_bf16 v[38:41], v[150:153], v[202:205], v[38:41]
	v_mfma_f32_16x16x32_bf16 v[34:37], v[158:161], v[202:205], v[34:37]
	v_mfma_f32_16x16x32_bf16 v[22:25], v[150:153], v[212:215], v[22:25]
	v_mfma_f32_16x16x32_bf16 v[18:21], v[158:161], v[212:215], v[18:21]
	v_mfma_f32_16x16x32_bf16 v[10:13], v[150:153], v[220:223], v[10:13]
	v_mfma_f32_16x16x32_bf16 v[2:5], v[158:161], v[220:223], v[2:5]
	s_setprio 0
	s_barrier
	s_add_u32 s56, s56, 0x100
	s_addc_u32 s57, s57, 0
	s_add_u32 s93, s93, 0x100
	s_addc_u32 s94, s94, 0
	s_cmp_ge_i32 s95, s76
	s_cselect_b32 s99, 0, 1
	s_mov_b32 s58, s95
	s_cbranch_scc0 .LBB0_1070
	v_readlane_b32 s94, v254, 5
	v_readlane_b32 s95, v254, 6

; #define PG8_STAGE(bufoff, gbase, voff) do { _Pragma("unroll") for (int _i = 0; _i < 2; ++_i) \
;         __builtin_amdgcn_global_load_lds((const unsigned*)((const char*)(gbase) + (voff)[_i]), (PG8_LAS unsigned*)(lds + (bufoff) + ldsw + _i * 8192), 16, 0, 0); } while (0)
; #define PG8_LDA(dst, b, h) do { _Pragma("unroll") for (int m = 0; m < 4; ++m) { const bf16x8 f0_ = *(const PG8_LAS bf16x8*)(lds + PG8_SA(b, h) + aoff + m * 2048), f1_ = *(const PG8_LAS bf16x8*)(lds + PG8_SA(b, h) + aoff + m * 2048 + 1024); dst[m].set(f0_, f1_); } } while (0)
; #define PG8_LDB(dst, b, h) do { _Pragma("unroll") for (int n = 0; n < 2; ++n) { const bf16x8 f0_ = *(const PG8_LAS bf16x8*)(lds + PG8_SB(b, h) + boff + n * 2048), f1_ = *(const PG8_LAS bf16x8*)(lds + PG8_SB(b, h) + boff + n * 2048 + 1024); dst[n].set(f0_, f1_); } } while (0)
; #define PG8_WAIT_V(n) asm volatile("s_waitcnt vmcnt(" #n ")" ::: "memory")
; #define PG8_WAIT_L(n) asm volatile("s_waitcnt lgkmcnt(" #n ")" ::: "memory")
; #define PG8_BAR __builtin_amdgcn_s_barrier()
; #define PG8_SCHED __builtin_amdgcn_sched_barrier(0)
; template <class Epi, class Sched, bool ALIGN_EPI = false, bool SP2 = false>
; __device__ __forceinline__ void gemm_phase(PG8_LAS unsigned char* lds, const Gemm g, const Sched& S, const Epi& E) {
;     ...
;             const bool last = (t == nt - 2);
;             const char* a1 = cA + (size_t)(t + 1) * kstep;
;             const char* a2 = last ? nA : cA + (size_t)(t + 2) * kstep; const char* b2 = last ? nB : cB + (size_t)(t + 2) * kstep;
;             const char* a3 = a2 + kstep; const char* b3 = b2 + kstep;
;             if (last && has_next) S.a_ready(nxt);
;             if constexpr (SP2) {
;             PG8_LDB(B0, 0, 0); PG8_LDB(B1, 0, 1); PG8_SCHED; PG8_LDA(At, 0, 0); PG8_STAGE(PG8_SA(1, 1), a1 + hstep, voffA);
;             PG8_WAIT_V(8); PG8_WAIT_L(0); PG8_BAR; PG8_MMA(0, 0, At, B0); PG8_MMA(0, 1, At, B1); PG8_BAR; PG8_SCHED;
;             PG8_LDA(At, 0, 1); PG8_STAGE(PG8_SB(0, 0), b2, voffB); PG8_STAGE(PG8_SB(0, 1), b2 + hstepB, voffB); PG8_STAGE(PG8_SA(0, 0), a2, voffA);
;             PG8_WAIT_V(8); PG8_WAIT_L(0); PG8_BAR; PG8_MMA(1, 0, At, B0); PG8_MMA(1, 1, At, B1); PG8_BAR; PG8_SCHED;
.LBB0_1171:
	ds_read_b128 v[156:159], v152
	ds_read_b128 v[160:163], v152 offset:1024
	ds_read_b128 v[164:167], v152 offset:2048
	ds_read_b128 v[168:171], v152 offset:3072
	ds_read_b128 v[172:175], v153
	ds_read_b128 v[176:179], v153 offset:1024
	ds_read_b128 v[180:183], v153 offset:2048
	ds_read_b128 v[184:187], v153 offset:3072
	s_add_i32 s61, s34, 2
	s_add_u32 s0, s30, 0x80
	s_addc_u32 s1, s31, 0
	s_cmp_eq_u32 s49, s34
	s_cselect_b32 s34, s6, s0
	s_cselect_b32 s35, s7, s1
	s_cselect_b32 s1, s29, s59
	s_cselect_b32 s0, s28, s58
	s_cmp_eq_u32 s99, 0
	s_cbranch_scc1 .Lkr3_a
	v_lshl_add_u64 v[228:229], v[228:229], 0, s[22:23]
	s_mov_b32 m0, s45
	v_lshl_add_u64 v[230:231], v[230:231], 0, s[22:23]
	global_load_lds_dwordx4 v[228:229], off
	s_mov_b32 m0, s46
	s_nop 0
	global_load_lds_dwordx4 v[230:231], off
.Lkr3_a:
	v_lshl_add_u64 v[148:149], s[30:31], 0, v[140:141]
	s_add_i32 m0, s40, 0xc000
	ds_read_b128 v[188:191], v154
	ds_read_b128 v[192:195], v154 offset:1024
	ds_read_b128 v[196:199], v154 offset:2048
	ds_read_b128 v[200:203], v154 offset:3072
	ds_read_b128 v[204:207], v154 offset:4096
	ds_read_b128 v[212:215], v154 offset:5120
	ds_read_b128 v[216:219], v154 offset:6144
	ds_read_b128 v[220:223], v154 offset:7168
	global_load_lds_dwordx4 v[148:149], off
	v_lshl_add_u64 v[148:149], s[30:31], 0, v[142:143]
	s_add_i32 m0, s40, 0xe000
	s_nop 0
	global_load_lds_dwordx4 v[148:149], off
	s_waitcnt vmcnt(8)
	s_waitcnt lgkmcnt(0)
	s_barrier
	s_setprio 1
	s_waitcnt lgkmcnt(0)
	v_mfma_f32_16x16x32_bf16 v[126:129], v[156:159], v[188:191], v[126:129]
	v_mfma_f32_16x16x32_bf16 v[122:125], v[164:167], v[188:191], v[122:125]
	v_mfma_f32_16x16x32_bf16 v[110:113], v[156:159], v[196:199], v[110:113]
	v_mfma_f32_16x16x32_bf16 v[106:109], v[164:167], v[196:199], v[106:109]
	v_mfma_f32_16x16x32_bf16 v[94:97], v[156:159], v[204:207], v[94:97]
	v_mfma_f32_16x16x32_bf16 v[90:93], v[164:167], v[204:207], v[90:93]
	v_mfma_f32_16x16x32_bf16 v[78:81], v[156:159], v[216:219], v[78:81]
	v_mfma_f32_16x16x32_bf16 v[74:77], v[164:167], v[216:219], v[74:77]
	v_mfma_f32_16x16x32_bf16 v[126:129], v[160:163], v[192:195], v[126:129]
	v_mfma_f32_16x16x32_bf16 v[122:125], v[168:171], v[192:195], v[122:125]
	v_mfma_f32_16x16x32_bf16 v[110:113], v[160:163], v[200:203], v[110:113]
	v_mfma_f32_16x16x32_bf16 v[106:109], v[168:171], v[200:203], v[106:109]
	v_mfma_f32_16x16x32_bf16 v[94:97], v[160:163], v[212:215], v[94:97]
	v_mfma_f32_16x16x32_bf16 v[90:93], v[168:171], v[212:215], v[90:93]
	v_mfma_f32_16x16x32_bf16 v[78:81], v[160:163], v[220:223], v[78:81]
	v_mfma_f32_16x16x32_bf16 v[74:77], v[168:171], v[220:223], v[74:77]
	s_setprio 0
	s_setprio 1
	v_mfma_f32_16x16x32_bf16 v[118:121], v[172:175], v[188:191], v[118:121]
	v_mfma_f32_16x16x32_bf16 v[114:117], v[180:183], v[188:191], v[114:117]
	v_mfma_f32_16x16x32_bf16 v[102:105], v[172:175], v[196:199], v[102:105]
	v_mfma_f32_16x16x32_bf16 v[98:101], v[180:183], v[196:199], v[98:101]
	v_mfma_f32_16x16x32_bf16 v[86:89], v[172:175], v[204:207], v[86:89]
	v_mfma_f32_16x16x32_bf16 v[82:85], v[180:183], v[204:207], v[82:85]
	v_mfma_f32_16x16x32_bf16 v[70:73], v[172:175], v[216:219], v[70:73]
	v_mfma_f32_16x16x32_bf16 v[66:69], v[180:183], v[216:219], v[66:69]
	v_mfma_f32_16x16x32_bf16 v[118:121], v[176:179], v[192:195], v[118:121]
	v_mfma_f32_16x16x32_bf16 v[114:117], v[184:187], v[192:195], v[114:117]
	v_mfma_f32_16x16x32_bf16 v[102:105], v[176:179], v[200:203], v[102:105]
	v_mfma_f32_16x16x32_bf16 v[98:101], v[184:187], v[200:203], v[98:101]
	v_mfma_f32_16x16x32_bf16 v[86:89], v[176:179], v[212:215], v[86:89]
	v_mfma_f32_16x16x32_bf16 v[82:85], v[184:187], v[212:215], v[82:85]
	v_mfma_f32_16x16x32_bf16 v[70:73], v[176:179], v[220:223], v[70:73]
	v_mfma_f32_16x16x32_bf16 v[66:69], v[184:187], v[220:223], v[66:69]
	s_setprio 0
	s_barrier
	s_add_i32 s33, s52, s39
	v_lshl_add_u64 v[148:149], s[0:1], 0, v[132:133]
	s_mov_b32 m0, s33
	ds_read_b128 v[188:191], v154 offset:16384
	ds_read_b128 v[192:195], v154 offset:17408
	ds_read_b128 v[196:199], v154 offset:18432
	ds_read_b128 v[200:203], v154 offset:19456
	ds_read_b128 v[204:207], v154 offset:20480
	ds_read_b128 v[212:215], v154 offset:21504
	ds_read_b128 v[216:219], v154 offset:22528
	ds_read_b128 v[220:223], v154 offset:23552
	global_load_lds_dwordx4 v[148:149], off
	s_add_i32 m0, s33, 0x2000
	v_lshl_add_u64 v[208:209], s[0:1], 0, v[136:137]
	s_add_u32 s0, s0, s14
	s_addc_u32 s1, s1, s15
	s_add_i32 s33, s53, s39
	global_load_lds_dwordx4 v[208:209], off
	v_lshl_add_u64 v[224:225], s[0:1], 0, v[132:133]
	s_mov_b32 m0, s33
	v_lshl_add_u64 v[226:227], s[0:1], 0, v[136:137]
	global_load_lds_dwordx4 v[224:225], off
	s_add_i32 m0, s33, 0x2000
	v_lshl_add_u64 v[228:229], s[34:35], 0, v[130:131]
	global_load_lds_dwordx4 v[226:227], off
	v_lshl_add_u64 v[230:231], s[34:35], 0, v[134:135]
	s_waitcnt vmcnt(6)
	s_waitcnt lgkmcnt(0)
	s_barrier
; #define PG8_STAGE(bufoff, gbase, voff) do { _Pragma("unroll") for (int _i = 0; _i < 2; ++_i) \
;         __builtin_amdgcn_global_load_lds((const unsigned*)((const char*)(gbase) + (voff)[_i]), (PG8_LAS unsigned*)(lds + (bufoff) + ldsw + _i * 8192), 16, 0, 0); } while (0)
; #define PG8_LDA(dst, b, h) do { _Pragma("unroll") for (int m = 0; m < 4; ++m) { const bf16x8 f0_ = *(const PG8_LAS bf16x8*)(lds + PG8_SA(b, h) + aoff + m * 2048), f1_ = *(const PG8_LAS bf16x8*)(lds + PG8_SA(b, h) + aoff + m * 2048 + 1024); dst[m].set(f0_, f1_); } } while (0)
; #define PG8_LDB(dst, b, h) do { _Pragma("unroll") for (int n = 0; n < 2; ++n) { const bf16x8 f0_ = *(const PG8_LAS bf16x8*)(lds + PG8_SB(b, h) + boff + n * 2048), f1_ = *(const PG8_LAS bf16x8*)(lds + PG8_SB(b, h) + boff + n * 2048 + 1024); dst[n].set(f0_, f1_); } } while (0)
; #define PG8_WAIT_V(n) asm volatile("s_waitcnt vmcnt(" #n ")" ::: "memory")
; #define PG8_WAIT_L(n) asm volatile("s_waitcnt lgkmcnt(" #n ")" ::: "memory")
; #define PG8_BAR __builtin_amdgcn_s_barrier()
; #define PG8_SCHED __builtin_amdgcn_sched_barrier(0)
; template <class Epi, class Sched, bool ALIGN_EPI = false, bool SP2 = false>
; __device__ __forceinline__ void gemm_phase(PG8_LAS unsigned char* lds, const Gemm g, const Sched& S, const Epi& E) {
;     ...
;             PG8_WAIT_V(8); PG8_WAIT_L(0); PG8_BAR; PG8_MMA(1, 0, At, B0); PG8_MMA(1, 1, At, B1); PG8_BAR; PG8_SCHED;
;             PG8_LDB(B0, 1, 0); PG8_LDB(B1, 1, 1); PG8_SCHED; PG8_LDA(At, 1, 0); PG8_STAGE(PG8_SA(0, 1), a2 + hstep, voffA);
;             PG8_WAIT_V(8); PG8_WAIT_L(0); PG8_BAR; PG8_MMA(0, 0, At, B0); PG8_MMA(0, 1, At, B1); PG8_BAR; PG8_SCHED;
	s_setprio 1
	s_waitcnt lgkmcnt(0)
	v_mfma_f32_16x16x32_bf16 v[62:65], v[156:159], v[188:191], v[62:65]
	v_mfma_f32_16x16x32_bf16 v[58:61], v[164:167], v[188:191], v[58:61]
	v_mfma_f32_16x16x32_bf16 v[46:49], v[156:159], v[196:199], v[46:49]
	v_mfma_f32_16x16x32_bf16 v[42:45], v[164:167], v[196:199], v[42:45]
	v_mfma_f32_16x16x32_bf16 v[30:33], v[156:159], v[204:207], v[30:33]
	v_mfma_f32_16x16x32_bf16 v[26:29], v[164:167], v[204:207], v[26:29]
	v_mfma_f32_16x16x32_bf16 v[14:17], v[156:159], v[216:219], v[14:17]
	v_mfma_f32_16x16x32_bf16 v[6:9], v[164:167], v[216:219], v[6:9]
	v_mfma_f32_16x16x32_bf16 v[62:65], v[160:163], v[192:195], v[62:65]
	v_mfma_f32_16x16x32_bf16 v[58:61], v[168:171], v[192:195], v[58:61]
	v_mfma_f32_16x16x32_bf16 v[46:49], v[160:163], v[200:203], v[46:49]
	v_mfma_f32_16x16x32_bf16 v[42:45], v[168:171], v[200:203], v[42:45]
	v_mfma_f32_16x16x32_bf16 v[30:33], v[160:163], v[212:215], v[30:33]
	v_mfma_f32_16x16x32_bf16 v[26:29], v[168:171], v[212:215], v[26:29]
	v_mfma_f32_16x16x32_bf16 v[14:17], v[160:163], v[220:223], v[14:17]
	v_mfma_f32_16x16x32_bf16 v[6:9], v[168:171], v[220:223], v[6:9]
	s_setprio 0
	s_setprio 1
	v_mfma_f32_16x16x32_bf16 v[54:57], v[172:175], v[188:191], v[54:57]
	v_mfma_f32_16x16x32_bf16 v[50:53], v[180:183], v[188:191], v[50:53]
	v_mfma_f32_16x16x32_bf16 v[38:41], v[172:175], v[196:199], v[38:41]
	v_mfma_f32_16x16x32_bf16 v[34:37], v[180:183], v[196:199], v[34:37]
	v_mfma_f32_16x16x32_bf16 v[22:25], v[172:175], v[204:207], v[22:25]
	v_mfma_f32_16x16x32_bf16 v[18:21], v[180:183], v[204:207], v[18:21]
	v_mfma_f32_16x16x32_bf16 v[10:13], v[172:175], v[216:219], v[10:13]
	v_mfma_f32_16x16x32_bf16 v[2:5], v[180:183], v[216:219], v[2:5]
	v_mfma_f32_16x16x32_bf16 v[54:57], v[176:179], v[192:195], v[54:57]
	v_mfma_f32_16x16x32_bf16 v[50:53], v[184:187], v[192:195], v[50:53]
	v_mfma_f32_16x16x32_bf16 v[38:41], v[176:179], v[200:203], v[38:41]
	v_mfma_f32_16x16x32_bf16 v[34:37], v[184:187], v[200:203], v[34:37]
	v_mfma_f32_16x16x32_bf16 v[22:25], v[176:179], v[212:215], v[22:25]
	v_mfma_f32_16x16x32_bf16 v[18:21], v[184:187], v[212:215], v[18:21]
	v_mfma_f32_16x16x32_bf16 v[10:13], v[176:179], v[220:223], v[10:13]
	v_mfma_f32_16x16x32_bf16 v[2:5], v[184:187], v[220:223], v[2:5]
	s_setprio 0
	s_barrier
	s_add_i32 s33, 0, 0x18000
	s_add_i32 s63, 0, 0x1c000
	v_add_u32_e32 v168, s33, v1
	v_add_u32_e32 v184, s63, v1
	ds_read_b128 v[156:159], v168
	ds_read_b128 v[160:163], v168 offset:1024
	ds_read_b128 v[164:167], v168 offset:2048
	ds_read_b128 v[168:171], v168 offset:3072
	ds_read_b128 v[172:175], v184
	ds_read_b128 v[176:179], v184 offset:1024
	ds_read_b128 v[180:183], v184 offset:2048
	ds_read_b128 v[184:187], v184 offset:3072
	s_add_u32 s0, s34, s12
	s_addc_u32 s1, s35, s13
	s_mov_b32 m0, s42
	v_lshl_add_u64 v[232:233], s[0:1], 0, v[130:131]
	ds_read_b128 v[188:191], v154 offset:32768
	ds_read_b128 v[192:195], v154 offset:33792
	ds_read_b128 v[196:199], v154 offset:34816
	ds_read_b128 v[200:203], v154 offset:35840
	ds_read_b128 v[204:207], v154 offset:36864
	ds_read_b128 v[212:215], v154 offset:37888
	ds_read_b128 v[216:219], v154 offset:38912
	ds_read_b128 v[220:223], v154 offset:39936
	s_mov_b32 m0, s40
	s_nop 0
	global_load_lds_dwordx4 v[228:229], off
	s_mov_b32 m0, s41
	s_nop 0
	global_load_lds_dwordx4 v[230:231], off
	s_mov_b32 m0, s42
	s_nop 0
	global_load_lds_dwordx4 v[232:233], off
	v_lshl_add_u64 v[232:233], s[0:1], 0, v[134:135]
	s_mov_b32 m0, s43
	s_nop 0
	global_load_lds_dwordx4 v[232:233], off
	s_waitcnt vmcnt(8)
	s_waitcnt lgkmcnt(0)
	s_barrier
	s_setprio 1
	s_waitcnt lgkmcnt(0)
	v_mfma_f32_16x16x32_bf16 v[126:129], v[156:159], v[188:191], v[126:129]
	v_mfma_f32_16x16x32_bf16 v[122:125], v[164:167], v[188:191], v[122:125]
	v_mfma_f32_16x16x32_bf16 v[110:113], v[156:159], v[196:199], v[110:113]
	v_mfma_f32_16x16x32_bf16 v[106:109], v[164:167], v[196:199], v[106:109]
	v_mfma_f32_16x16x32_bf16 v[94:97], v[156:159], v[204:207], v[94:97]
	v_mfma_f32_16x16x32_bf16 v[90:93], v[164:167], v[204:207], v[90:93]
	v_mfma_f32_16x16x32_bf16 v[78:81], v[156:159], v[216:219], v[78:81]
	v_mfma_f32_16x16x32_bf16 v[74:77], v[164:167], v[216:219], v[74:77]
	v_mfma_f32_16x16x32_bf16 v[126:129], v[160:163], v[192:195], v[126:129]
	v_mfma_f32_16x16x32_bf16 v[122:125], v[168:171], v[192:195], v[122:125]
	v_mfma_f32_16x16x32_bf16 v[110:113], v[160:163], v[200:203], v[110:113]
	v_mfma_f32_16x16x32_bf16 v[106:109], v[168:171], v[200:203], v[106:109]
	v_mfma_f32_16x16x32_bf16 v[94:97], v[160:163], v[212:215], v[94:97]
	v_mfma_f32_16x16x32_bf16 v[90:93], v[168:171], v[212:215], v[90:93]
	v_mfma_f32_16x16x32_bf16 v[78:81], v[160:163], v[220:223], v[78:81]
	v_mfma_f32_16x16x32_bf16 v[74:77], v[168:171], v[220:223], v[74:77]
	s_setprio 0
	s_setprio 1
	v_mfma_f32_16x16x32_bf16 v[118:121], v[172:175], v[188:191], v[118:121]
	v_mfma_f32_16x16x32_bf16 v[114:117], v[180:183], v[188:191], v[114:117]
	v_mfma_f32_16x16x32_bf16 v[102:105], v[172:175], v[196:199], v[102:105]
	v_mfma_f32_16x16x32_bf16 v[98:101], v[180:183], v[196:199], v[98:101]
	v_mfma_f32_16x16x32_bf16 v[86:89], v[172:175], v[204:207], v[86:89]
	v_mfma_f32_16x16x32_bf16 v[82:85], v[180:183], v[204:207], v[82:85]
	v_mfma_f32_16x16x32_bf16 v[70:73], v[172:175], v[216:219], v[70:73]
	v_mfma_f32_16x16x32_bf16 v[66:69], v[180:183], v[216:219], v[66:69]
	v_mfma_f32_16x16x32_bf16 v[118:121], v[176:179], v[192:195], v[118:121]
	v_mfma_f32_16x16x32_bf16 v[114:117], v[184:187], v[192:195], v[114:117]
	v_mfma_f32_16x16x32_bf16 v[102:105], v[176:179], v[200:203], v[102:105]
	v_mfma_f32_16x16x32_bf16 v[98:101], v[184:187], v[200:203], v[98:101]
	v_mfma_f32_16x16x32_bf16 v[86:89], v[176:179], v[212:215], v[86:89]
	v_mfma_f32_16x16x32_bf16 v[82:85], v[184:187], v[212:215], v[82:85]
	v_mfma_f32_16x16x32_bf16 v[70:73], v[176:179], v[220:223], v[70:73]
	v_mfma_f32_16x16x32_bf16 v[66:69], v[184:187], v[220:223], v[66:69]
	s_setprio 0
	s_barrier
; #define PG8_STAGE(bufoff, gbase, voff) do { _Pragma("unroll") for (int _i = 0; _i < 2; ++_i) \
;         __builtin_amdgcn_global_load_lds((const unsigned*)((const char*)(gbase) + (voff)[_i]), (PG8_LAS unsigned*)(lds + (bufoff) + ldsw + _i * 8192), 16, 0, 0); } while (0)
; #define PG8_LDA(dst, b, h) do { _Pragma("unroll") for (int m = 0; m < 4; ++m) { const bf16x8 f0_ = *(const PG8_LAS bf16x8*)(lds + PG8_SA(b, h) + aoff + m * 2048), f1_ = *(const PG8_LAS bf16x8*)(lds + PG8_SA(b, h) + aoff + m * 2048 + 1024); dst[m].set(f0_, f1_); } } while (0)
; #define PG8_WAIT_V(n) asm volatile("s_waitcnt vmcnt(" #n ")" ::: "memory")
; #define PG8_WAIT_L(n) asm volatile("s_waitcnt lgkmcnt(" #n ")" ::: "memory")
; #define PG8_BAR __builtin_amdgcn_s_barrier()
; #define PG8_SCHED __builtin_amdgcn_sched_barrier(0)
; template <class Epi, class Sched, bool ALIGN_EPI = false, bool SP2 = false>
; __device__ __forceinline__ void gemm_phase(PG8_LAS unsigned char* lds, const Gemm g, const Sched& S, const Epi& E) {
;     ...
;             PG8_LDA(At, 1, 1); PG8_STAGE(PG8_SB(1, 0), b3, voffB); PG8_STAGE(PG8_SB(1, 1), b3 + hstepB, voffB); PG8_STAGE(PG8_SA(1, 0), a3, voffA);
;             PG8_WAIT_V(8); PG8_WAIT_L(0); PG8_BAR; PG8_MMA(1, 0, At, B0); PG8_MMA(1, 1, At, B1); PG8_BAR; PG8_SCHED;
	s_add_i32 s0, s33, s39
	v_lshl_add_u64 v[148:149], v[148:149], 0, s[22:23]
	s_mov_b32 m0, s0
	ds_read_b128 v[188:191], v154 offset:49152
	ds_read_b128 v[192:195], v154 offset:50176
	ds_read_b128 v[196:199], v154 offset:51200
	ds_read_b128 v[200:203], v154 offset:52224
	ds_read_b128 v[204:207], v154 offset:53248
	ds_read_b128 v[212:215], v154 offset:54272
	ds_read_b128 v[216:219], v154 offset:55296
	ds_read_b128 v[220:223], v154 offset:56320
	global_load_lds_dwordx4 v[148:149], off
	v_lshl_add_u64 v[148:149], v[208:209], 0, s[22:23]
	s_add_i32 m0, s0, 0x2000
	s_add_i32 s0, s63, s39
	global_load_lds_dwordx4 v[148:149], off
	v_lshl_add_u64 v[148:149], v[224:225], 0, s[22:23]
	s_mov_b32 m0, s0
	s_nop 0
	global_load_lds_dwordx4 v[148:149], off
	v_lshl_add_u64 v[148:149], v[226:227], 0, s[22:23]
	s_add_i32 m0, s0, 0x2000
	s_nop 0
	global_load_lds_dwordx4 v[148:149], off
	s_cmp_ge_i32 s61, s47
	s_cbranch_scc0 .Lkr3_b
	v_lshl_add_u64 v[148:149], v[228:229], 0, s[22:23]
	s_mov_b32 m0, s45
	s_nop 0
	global_load_lds_dwordx4 v[148:149], off
	v_lshl_add_u64 v[148:149], v[230:231], 0, s[22:23]
	s_mov_b32 m0, s46
	s_nop 0
	global_load_lds_dwordx4 v[148:149], off
.Lkr3_b:
	s_waitcnt vmcnt(6)
	s_waitcnt lgkmcnt(0)
	s_barrier
	s_setprio 1
	s_waitcnt lgkmcnt(0)
	v_mfma_f32_16x16x32_bf16 v[62:65], v[156:159], v[188:191], v[62:65]
	v_mfma_f32_16x16x32_bf16 v[58:61], v[164:167], v[188:191], v[58:61]
	v_mfma_f32_16x16x32_bf16 v[46:49], v[156:159], v[196:199], v[46:49]
	v_mfma_f32_16x16x32_bf16 v[42:45], v[164:167], v[196:199], v[42:45]
	v_mfma_f32_16x16x32_bf16 v[30:33], v[156:159], v[204:207], v[30:33]
	v_mfma_f32_16x16x32_bf16 v[26:29], v[164:167], v[204:207], v[26:29]
	v_mfma_f32_16x16x32_bf16 v[14:17], v[156:159], v[216:219], v[14:17]
	v_mfma_f32_16x16x32_bf16 v[6:9], v[164:167], v[216:219], v[6:9]
	v_mfma_f32_16x16x32_bf16 v[62:65], v[160:163], v[192:195], v[62:65]
	v_mfma_f32_16x16x32_bf16 v[58:61], v[168:171], v[192:195], v[58:61]
	v_mfma_f32_16x16x32_bf16 v[46:49], v[160:163], v[200:203], v[46:49]
	v_mfma_f32_16x16x32_bf16 v[42:45], v[168:171], v[200:203], v[42:45]
	v_mfma_f32_16x16x32_bf16 v[30:33], v[160:163], v[212:215], v[30:33]
	v_mfma_f32_16x16x32_bf16 v[26:29], v[168:171], v[212:215], v[26:29]
	v_mfma_f32_16x16x32_bf16 v[14:17], v[160:163], v[220:223], v[14:17]
	v_mfma_f32_16x16x32_bf16 v[6:9], v[168:171], v[220:223], v[6:9]
	s_setprio 0
	s_setprio 1
	v_mfma_f32_16x16x32_bf16 v[54:57], v[172:175], v[188:191], v[54:57]
	v_mfma_f32_16x16x32_bf16 v[50:53], v[180:183], v[188:191], v[50:53]
	v_mfma_f32_16x16x32_bf16 v[38:41], v[172:175], v[196:199], v[38:41]
	v_mfma_f32_16x16x32_bf16 v[34:37], v[180:183], v[196:199], v[34:37]
	v_mfma_f32_16x16x32_bf16 v[22:25], v[172:175], v[204:207], v[22:25]
	v_mfma_f32_16x16x32_bf16 v[18:21], v[180:183], v[204:207], v[18:21]
	v_mfma_f32_16x16x32_bf16 v[10:13], v[172:175], v[216:219], v[10:13]
	v_mfma_f32_16x16x32_bf16 v[2:5], v[180:183], v[216:219], v[2:5]
	v_mfma_f32_16x16x32_bf16 v[54:57], v[176:179], v[192:195], v[54:57]
	v_mfma_f32_16x16x32_bf16 v[50:53], v[184:187], v[192:195], v[50:53]
	v_mfma_f32_16x16x32_bf16 v[38:41], v[176:179], v[200:203], v[38:41]
	v_mfma_f32_16x16x32_bf16 v[34:37], v[184:187], v[200:203], v[34:37]
	v_mfma_f32_16x16x32_bf16 v[22:25], v[176:179], v[212:215], v[22:25]
	v_mfma_f32_16x16x32_bf16 v[18:21], v[184:187], v[212:215], v[18:21]
	v_mfma_f32_16x16x32_bf16 v[10:13], v[176:179], v[220:223], v[10:13]
	v_mfma_f32_16x16x32_bf16 v[2:5], v[184:187], v[220:223], v[2:5]
	s_setprio 0
	s_barrier
	s_add_u32 s30, s30, 0x100
	s_addc_u32 s31, s31, 0
	s_add_u32 s58, s58, 0x100
	s_addc_u32 s59, s59, 0
	s_cmp_ge_i32 s61, s47
	s_cselect_b32 s99, 0, 1
	s_mov_b32 s34, s61
	s_cbranch_scc0 .LBB0_1171

; #define PG8_STAGE(bufoff, gbase, voff) do { _Pragma("unroll") for (int _i = 0; _i < 2; ++_i) \
;         __builtin_amdgcn_global_load_lds((const unsigned*)((const char*)(gbase) + (voff)[_i]), (PG8_LAS unsigned*)(lds + (bufoff) + ldsw + _i * 8192), 16, 0, 0); } while (0)
; #define PG8_LDA(dst, b, h) do { _Pragma("unroll") for (int m = 0; m < 4; ++m) { const bf16x8 f0_ = *(const PG8_LAS bf16x8*)(lds + PG8_SA(b, h) + aoff + m * 2048), f1_ = *(const PG8_LAS bf16x8*)(lds + PG8_SA(b, h) + aoff + m * 2048 + 1024); dst[m].set(f0_, f1_); } } while (0)
; #define PG8_LDB(dst, b, h) do { _Pragma("unroll") for (int n = 0; n < 2; ++n) { const bf16x8 f0_ = *(const PG8_LAS bf16x8*)(lds + PG8_SB(b, h) + boff + n * 2048), f1_ = *(const PG8_LAS bf16x8*)(lds + PG8_SB(b, h) + boff + n * 2048 + 1024); dst[n].set(f0_, f1_); } } while (0)
; #define PG8_WAIT_V(n) asm volatile("s_waitcnt vmcnt(" #n ")" ::: "memory")
; #define PG8_WAIT_L(n) asm volatile("s_waitcnt lgkmcnt(" #n ")" ::: "memory")
; #define PG8_BAR __builtin_amdgcn_s_barrier()
; #define PG8_SCHED __builtin_amdgcn_sched_barrier(0)
; template <class Epi, class Sched, bool ALIGN_EPI = false, bool SP2 = false>
; __device__ __forceinline__ void gemm_phase(PG8_LAS unsigned char* lds, const Gemm g, const Sched& S, const Epi& E) {
;     ...
;             const bool last = (t == nt - 2);
;             const char* a1 = cA + (size_t)(t + 1) * kstep;
;             const char* a2 = last ? nA : cA + (size_t)(t + 2) * kstep; const char* b2 = last ? nB : cB + (size_t)(t + 2) * kstep;
;             const char* a3 = a2 + kstep; const char* b3 = b2 + kstep;
;             if (last && has_next) S.a_ready(nxt);
;             if constexpr (SP2) {
;             PG8_LDB(B0, 0, 0); PG8_LDB(B1, 0, 1); PG8_SCHED; PG8_LDA(At, 0, 0); PG8_STAGE(PG8_SA(1, 1), a1 + hstep, voffA);
;             PG8_WAIT_V(8); PG8_WAIT_L(0); PG8_BAR; PG8_MMA(0, 0, At, B0); PG8_MMA(0, 1, At, B1); PG8_BAR; PG8_SCHED;
;             PG8_LDA(At, 0, 1); PG8_STAGE(PG8_SB(0, 0), b2, voffB); PG8_STAGE(PG8_SB(0, 1), b2 + hstepB, voffB); PG8_STAGE(PG8_SA(0, 0), a2, voffA);
;             PG8_WAIT_V(8); PG8_WAIT_L(0); PG8_BAR; PG8_MMA(1, 0, At, B0); PG8_MMA(1, 1, At, B1); PG8_BAR; PG8_SCHED;
.LBB0_1592:
	ds_read_b128 v[156:159], v152
	ds_read_b128 v[160:163], v152 offset:1024
	ds_read_b128 v[164:167], v152 offset:2048
	ds_read_b128 v[168:171], v152 offset:3072
	ds_read_b128 v[172:175], v153
	ds_read_b128 v[176:179], v153 offset:1024
	ds_read_b128 v[180:183], v153 offset:2048
	ds_read_b128 v[184:187], v153 offset:3072
	s_add_i32 s61, s34, 2
	s_add_u32 s0, s30, 0x80
	s_addc_u32 s1, s31, 0
	s_cmp_eq_u32 s49, s34
	s_cselect_b32 s34, s6, s0
	s_cselect_b32 s35, s7, s1
	s_cselect_b32 s1, s29, s59
	s_cselect_b32 s0, s28, s58
	s_cmp_eq_u32 s99, 0
	s_cbranch_scc1 .Lkr4_a
	v_lshl_add_u64 v[228:229], v[228:229], 0, s[22:23]
	s_mov_b32 m0, s46
	v_lshl_add_u64 v[230:231], v[230:231], 0, s[22:23]
	global_load_lds_dwordx4 v[228:229], off
	s_mov_b32 m0, s47
	s_nop 0
	global_load_lds_dwordx4 v[230:231], off
.Lkr4_a:
	v_lshl_add_u64 v[148:149], s[30:31], 0, v[140:141]
	s_add_i32 m0, s40, 0xc000
	ds_read_b128 v[188:191], v154
	ds_read_b128 v[192:195], v154 offset:1024
	ds_read_b128 v[196:199], v154 offset:2048
	ds_read_b128 v[200:203], v154 offset:3072
	ds_read_b128 v[204:207], v154 offset:4096
	ds_read_b128 v[212:215], v154 offset:5120
	ds_read_b128 v[216:219], v154 offset:6144
	ds_read_b128 v[220:223], v154 offset:7168
	global_load_lds_dwordx4 v[148:149], off
	v_lshl_add_u64 v[148:149], s[30:31], 0, v[142:143]
	s_add_i32 m0, s40, 0xe000
	s_nop 0
	global_load_lds_dwordx4 v[148:149], off
	s_waitcnt vmcnt(8)
	s_waitcnt lgkmcnt(0)
	s_barrier
	s_setprio 1
	s_waitcnt lgkmcnt(0)
	v_mfma_f32_16x16x32_bf16 v[126:129], v[156:159], v[188:191], v[126:129]
	v_mfma_f32_16x16x32_bf16 v[122:125], v[164:167], v[188:191], v[122:125]
	v_mfma_f32_16x16x32_bf16 v[110:113], v[156:159], v[196:199], v[110:113]
	v_mfma_f32_16x16x32_bf16 v[106:109], v[164:167], v[196:199], v[106:109]
	v_mfma_f32_16x16x32_bf16 v[94:97], v[156:159], v[204:207], v[94:97]
	v_mfma_f32_16x16x32_bf16 v[90:93], v[164:167], v[204:207], v[90:93]
	v_mfma_f32_16x16x32_bf16 v[78:81], v[156:159], v[216:219], v[78:81]
	v_mfma_f32_16x16x32_bf16 v[74:77], v[164:167], v[216:219], v[74:77]
	v_mfma_f32_16x16x32_bf16 v[126:129], v[160:163], v[192:195], v[126:129]
	v_mfma_f32_16x16x32_bf16 v[122:125], v[168:171], v[192:195], v[122:125]
	v_mfma_f32_16x16x32_bf16 v[110:113], v[160:163], v[200:203], v[110:113]
	v_mfma_f32_16x16x32_bf16 v[106:109], v[168:171], v[200:203], v[106:109]
	v_mfma_f32_16x16x32_bf16 v[94:97], v[160:163], v[212:215], v[94:97]
	v_mfma_f32_16x16x32_bf16 v[90:93], v[168:171], v[212:215], v[90:93]
	v_mfma_f32_16x16x32_bf16 v[78:81], v[160:163], v[220:223], v[78:81]
	v_mfma_f32_16x16x32_bf16 v[74:77], v[168:171], v[220:223], v[74:77]
	s_setprio 0
	s_setprio 1
	v_mfma_f32_16x16x32_bf16 v[118:121], v[172:175], v[188:191], v[118:121]
	v_mfma_f32_16x16x32_bf16 v[114:117], v[180:183], v[188:191], v[114:117]
	v_mfma_f32_16x16x32_bf16 v[102:105], v[172:175], v[196:199], v[102:105]
	v_mfma_f32_16x16x32_bf16 v[98:101], v[180:183], v[196:199], v[98:101]
	v_mfma_f32_16x16x32_bf16 v[86:89], v[172:175], v[204:207], v[86:89]
	v_mfma_f32_16x16x32_bf16 v[82:85], v[180:183], v[204:207], v[82:85]
	v_mfma_f32_16x16x32_bf16 v[70:73], v[172:175], v[216:219], v[70:73]
	v_mfma_f32_16x16x32_bf16 v[66:69], v[180:183], v[216:219], v[66:69]
	v_mfma_f32_16x16x32_bf16 v[118:121], v[176:179], v[192:195], v[118:121]
	v_mfma_f32_16x16x32_bf16 v[114:117], v[184:187], v[192:195], v[114:117]
	v_mfma_f32_16x16x32_bf16 v[102:105], v[176:179], v[200:203], v[102:105]
	v_mfma_f32_16x16x32_bf16 v[98:101], v[184:187], v[200:203], v[98:101]
	v_mfma_f32_16x16x32_bf16 v[86:89], v[176:179], v[212:215], v[86:89]
	v_mfma_f32_16x16x32_bf16 v[82:85], v[184:187], v[212:215], v[82:85]
	v_mfma_f32_16x16x32_bf16 v[70:73], v[176:179], v[220:223], v[70:73]
	v_mfma_f32_16x16x32_bf16 v[66:69], v[184:187], v[220:223], v[66:69]
	s_setprio 0
	s_barrier
	s_add_i32 s33, s52, s39
	v_lshl_add_u64 v[148:149], s[0:1], 0, v[132:133]
	s_mov_b32 m0, s33
	ds_read_b128 v[188:191], v154 offset:16384
	ds_read_b128 v[192:195], v154 offset:17408
	ds_read_b128 v[196:199], v154 offset:18432
	ds_read_b128 v[200:203], v154 offset:19456
	ds_read_b128 v[204:207], v154 offset:20480
	ds_read_b128 v[212:215], v154 offset:21504
	ds_read_b128 v[216:219], v154 offset:22528
	ds_read_b128 v[220:223], v154 offset:23552
	global_load_lds_dwordx4 v[148:149], off
	s_add_i32 m0, s33, 0x2000
	v_lshl_add_u64 v[208:209], s[0:1], 0, v[136:137]
	s_add_u32 s0, s0, s14
	s_addc_u32 s1, s1, s15
	s_add_i32 s33, s53, s39
	global_load_lds_dwordx4 v[208:209], off
	v_lshl_add_u64 v[224:225], s[0:1], 0, v[132:133]
	s_mov_b32 m0, s33
	v_lshl_add_u64 v[226:227], s[0:1], 0, v[136:137]
	global_load_lds_dwordx4 v[224:225], off
	s_add_i32 m0, s33, 0x2000
	v_lshl_add_u64 v[228:229], s[34:35], 0, v[130:131]
	global_load_lds_dwordx4 v[226:227], off
	v_lshl_add_u64 v[230:231], s[34:35], 0, v[134:135]
	s_waitcnt vmcnt(6)
	s_waitcnt lgkmcnt(0)
	s_barrier
; #define PG8_STAGE(bufoff, gbase, voff) do { _Pragma("unroll") for (int _i = 0; _i < 2; ++_i) \
;         __builtin_amdgcn_global_load_lds((const unsigned*)((const char*)(gbase) + (voff)[_i]), (PG8_LAS unsigned*)(lds + (bufoff) + ldsw + _i * 8192), 16, 0, 0); } while (0)
; #define PG8_LDA(dst, b, h) do { _Pragma("unroll") for (int m = 0; m < 4; ++m) { const bf16x8 f0_ = *(const PG8_LAS bf16x8*)(lds + PG8_SA(b, h) + aoff + m * 2048), f1_ = *(const PG8_LAS bf16x8*)(lds + PG8_SA(b, h) + aoff + m * 2048 + 1024); dst[m].set(f0_, f1_); } } while (0)
; #define PG8_LDB(dst, b, h) do { _Pragma("unroll") for (int n = 0; n < 2; ++n) { const bf16x8 f0_ = *(const PG8_LAS bf16x8*)(lds + PG8_SB(b, h) + boff + n * 2048), f1_ = *(const PG8_LAS bf16x8*)(lds + PG8_SB(b, h) + boff + n * 2048 + 1024); dst[n].set(f0_, f1_); } } while (0)
; #define PG8_WAIT_V(n) asm volatile("s_waitcnt vmcnt(" #n ")" ::: "memory")
; #define PG8_WAIT_L(n) asm volatile("s_waitcnt lgkmcnt(" #n ")" ::: "memory")
; #define PG8_BAR __builtin_amdgcn_s_barrier()
; #define PG8_SCHED __builtin_amdgcn_sched_barrier(0)
; template <class Epi, class Sched, bool ALIGN_EPI = false, bool SP2 = false>
; __device__ __forceinline__ void gemm_phase(PG8_LAS unsigned char* lds, const Gemm g, const Sched& S, const Epi& E) {
;     ...
;             PG8_WAIT_V(8); PG8_WAIT_L(0); PG8_BAR; PG8_MMA(1, 0, At, B0); PG8_MMA(1, 1, At, B1); PG8_BAR; PG8_SCHED;
;             PG8_LDB(B0, 1, 0); PG8_LDB(B1, 1, 1); PG8_SCHED; PG8_LDA(At, 1, 0); PG8_STAGE(PG8_SA(0, 1), a2 + hstep, voffA);
;             PG8_WAIT_V(8); PG8_WAIT_L(0); PG8_BAR; PG8_MMA(0, 0, At, B0); PG8_MMA(0, 1, At, B1); PG8_BAR; PG8_SCHED;
	s_setprio 1
	s_waitcnt lgkmcnt(0)
	v_mfma_f32_16x16x32_bf16 v[62:65], v[156:159], v[188:191], v[62:65]
	v_mfma_f32_16x16x32_bf16 v[58:61], v[164:167], v[188:191], v[58:61]
	v_mfma_f32_16x16x32_bf16 v[46:49], v[156:159], v[196:199], v[46:49]
	v_mfma_f32_16x16x32_bf16 v[42:45], v[164:167], v[196:199], v[42:45]
	v_mfma_f32_16x16x32_bf16 v[30:33], v[156:159], v[204:207], v[30:33]
	v_mfma_f32_16x16x32_bf16 v[26:29], v[164:167], v[204:207], v[26:29]
	v_mfma_f32_16x16x32_bf16 v[14:17], v[156:159], v[216:219], v[14:17]
	v_mfma_f32_16x16x32_bf16 v[6:9], v[164:167], v[216:219], v[6:9]
	v_mfma_f32_16x16x32_bf16 v[62:65], v[160:163], v[192:195], v[62:65]
	v_mfma_f32_16x16x32_bf16 v[58:61], v[168:171], v[192:195], v[58:61]
	v_mfma_f32_16x16x32_bf16 v[46:49], v[160:163], v[200:203], v[46:49]
	v_mfma_f32_16x16x32_bf16 v[42:45], v[168:171], v[200:203], v[42:45]
	v_mfma_f32_16x16x32_bf16 v[30:33], v[160:163], v[212:215], v[30:33]
	v_mfma_f32_16x16x32_bf16 v[26:29], v[168:171], v[212:215], v[26:29]
	v_mfma_f32_16x16x32_bf16 v[14:17], v[160:163], v[220:223], v[14:17]
	v_mfma_f32_16x16x32_bf16 v[6:9], v[168:171], v[220:223], v[6:9]
	s_setprio 0
	s_setprio 1
	v_mfma_f32_16x16x32_bf16 v[54:57], v[172:175], v[188:191], v[54:57]
	v_mfma_f32_16x16x32_bf16 v[50:53], v[180:183], v[188:191], v[50:53]
	v_mfma_f32_16x16x32_bf16 v[38:41], v[172:175], v[196:199], v[38:41]
	v_mfma_f32_16x16x32_bf16 v[34:37], v[180:183], v[196:199], v[34:37]
	v_mfma_f32_16x16x32_bf16 v[22:25], v[172:175], v[204:207], v[22:25]
	v_mfma_f32_16x16x32_bf16 v[18:21], v[180:183], v[204:207], v[18:21]
	v_mfma_f32_16x16x32_bf16 v[10:13], v[172:175], v[216:219], v[10:13]
	v_mfma_f32_16x16x32_bf16 v[2:5], v[180:183], v[216:219], v[2:5]
	v_mfma_f32_16x16x32_bf16 v[54:57], v[176:179], v[192:195], v[54:57]
	v_mfma_f32_16x16x32_bf16 v[50:53], v[184:187], v[192:195], v[50:53]
	v_mfma_f32_16x16x32_bf16 v[38:41], v[176:179], v[200:203], v[38:41]
	v_mfma_f32_16x16x32_bf16 v[34:37], v[184:187], v[200:203], v[34:37]
	v_mfma_f32_16x16x32_bf16 v[22:25], v[176:179], v[212:215], v[22:25]
	v_mfma_f32_16x16x32_bf16 v[18:21], v[184:187], v[212:215], v[18:21]
	v_mfma_f32_16x16x32_bf16 v[10:13], v[176:179], v[220:223], v[10:13]
	v_mfma_f32_16x16x32_bf16 v[2:5], v[184:187], v[220:223], v[2:5]
	s_setprio 0
	s_barrier
	s_add_i32 s33, 0, 0x18000
	s_add_i32 s63, 0, 0x1c000
	v_add_u32_e32 v168, s33, v1
	v_add_u32_e32 v184, s63, v1
	ds_read_b128 v[156:159], v168
	ds_read_b128 v[160:163], v168 offset:1024
	ds_read_b128 v[164:167], v168 offset:2048
	ds_read_b128 v[168:171], v168 offset:3072
	ds_read_b128 v[172:175], v184
	ds_read_b128 v[176:179], v184 offset:1024
	ds_read_b128 v[180:183], v184 offset:2048
	ds_read_b128 v[184:187], v184 offset:3072
	s_add_u32 s0, s34, s12
	s_addc_u32 s1, s35, s13
	s_mov_b32 m0, s42
	v_lshl_add_u64 v[232:233], s[0:1], 0, v[130:131]
	ds_read_b128 v[188:191], v154 offset:32768
	ds_read_b128 v[192:195], v154 offset:33792
	ds_read_b128 v[196:199], v154 offset:34816
	ds_read_b128 v[200:203], v154 offset:35840
	ds_read_b128 v[204:207], v154 offset:36864
	ds_read_b128 v[212:215], v154 offset:37888
	ds_read_b128 v[216:219], v154 offset:38912
	ds_read_b128 v[220:223], v154 offset:39936
	s_mov_b32 m0, s40
	s_nop 0
	global_load_lds_dwordx4 v[228:229], off
	s_mov_b32 m0, s41
	s_nop 0
	global_load_lds_dwordx4 v[230:231], off
	s_mov_b32 m0, s42
	s_nop 0
	global_load_lds_dwordx4 v[232:233], off
	v_lshl_add_u64 v[232:233], s[0:1], 0, v[134:135]
	s_mov_b32 m0, s43
	s_nop 0
	global_load_lds_dwordx4 v[232:233], off
	s_waitcnt vmcnt(8)
	s_waitcnt lgkmcnt(0)
	s_barrier
	s_setprio 1
	s_waitcnt lgkmcnt(0)
	v_mfma_f32_16x16x32_bf16 v[126:129], v[156:159], v[188:191], v[126:129]
	v_mfma_f32_16x16x32_bf16 v[122:125], v[164:167], v[188:191], v[122:125]
	v_mfma_f32_16x16x32_bf16 v[110:113], v[156:159], v[196:199], v[110:113]
	v_mfma_f32_16x16x32_bf16 v[106:109], v[164:167], v[196:199], v[106:109]
	v_mfma_f32_16x16x32_bf16 v[94:97], v[156:159], v[204:207], v[94:97]
	v_mfma_f32_16x16x32_bf16 v[90:93], v[164:167], v[204:207], v[90:93]
	v_mfma_f32_16x16x32_bf16 v[78:81], v[156:159], v[216:219], v[78:81]
	v_mfma_f32_16x16x32_bf16 v[74:77], v[164:167], v[216:219], v[74:77]
	v_mfma_f32_16x16x32_bf16 v[126:129], v[160:163], v[192:195], v[126:129]
	v_mfma_f32_16x16x32_bf16 v[122:125], v[168:171], v[192:195], v[122:125]
	v_mfma_f32_16x16x32_bf16 v[110:113], v[160:163], v[200:203], v[110:113]
	v_mfma_f32_16x16x32_bf16 v[106:109], v[168:171], v[200:203], v[106:109]
	v_mfma_f32_16x16x32_bf16 v[94:97], v[160:163], v[212:215], v[94:97]
	v_mfma_f32_16x16x32_bf16 v[90:93], v[168:171], v[212:215], v[90:93]
	v_mfma_f32_16x16x32_bf16 v[78:81], v[160:163], v[220:223], v[78:81]
	v_mfma_f32_16x16x32_bf16 v[74:77], v[168:171], v[220:223], v[74:77]
	s_setprio 0
	s_setprio 1
	v_mfma_f32_16x16x32_bf16 v[118:121], v[172:175], v[188:191], v[118:121]
	v_mfma_f32_16x16x32_bf16 v[114:117], v[180:183], v[188:191], v[114:117]
	v_mfma_f32_16x16x32_bf16 v[102:105], v[172:175], v[196:199], v[102:105]
	v_mfma_f32_16x16x32_bf16 v[98:101], v[180:183], v[196:199], v[98:101]
	v_mfma_f32_16x16x32_bf16 v[86:89], v[172:175], v[204:207], v[86:89]
	v_mfma_f32_16x16x32_bf16 v[82:85], v[180:183], v[204:207], v[82:85]
	v_mfma_f32_16x16x32_bf16 v[70:73], v[172:175], v[216:219], v[70:73]
	v_mfma_f32_16x16x32_bf16 v[66:69], v[180:183], v[216:219], v[66:69]
	v_mfma_f32_16x16x32_bf16 v[118:121], v[176:179], v[192:195], v[118:121]
	v_mfma_f32_16x16x32_bf16 v[114:117], v[184:187], v[192:195], v[114:117]
	v_mfma_f32_16x16x32_bf16 v[102:105], v[176:179], v[200:203], v[102:105]
	v_mfma_f32_16x16x32_bf16 v[98:101], v[184:187], v[200:203], v[98:101]
	v_mfma_f32_16x16x32_bf16 v[86:89], v[176:179], v[212:215], v[86:89]
	v_mfma_f32_16x16x32_bf16 v[82:85], v[184:187], v[212:215], v[82:85]
	v_mfma_f32_16x16x32_bf16 v[70:73], v[176:179], v[220:223], v[70:73]
	v_mfma_f32_16x16x32_bf16 v[66:69], v[184:187], v[220:223], v[66:69]
	s_setprio 0
	s_barrier
; #define PG8_STAGE(bufoff, gbase, voff) do { _Pragma("unroll") for (int _i = 0; _i < 2; ++_i) \
;         __builtin_amdgcn_global_load_lds((const unsigned*)((const char*)(gbase) + (voff)[_i]), (PG8_LAS unsigned*)(lds + (bufoff) + ldsw + _i * 8192), 16, 0, 0); } while (0)
; #define PG8_LDA(dst, b, h) do { _Pragma("unroll") for (int m = 0; m < 4; ++m) { const bf16x8 f0_ = *(const PG8_LAS bf16x8*)(lds + PG8_SA(b, h) + aoff + m * 2048), f1_ = *(const PG8_LAS bf16x8*)(lds + PG8_SA(b, h) + aoff + m * 2048 + 1024); dst[m].set(f0_, f1_); } } while (0)
; #define PG8_WAIT_V(n) asm volatile("s_waitcnt vmcnt(" #n ")" ::: "memory")
; #define PG8_WAIT_L(n) asm volatile("s_waitcnt lgkmcnt(" #n ")" ::: "memory")
; #define PG8_BAR __builtin_amdgcn_s_barrier()
; #define PG8_SCHED __builtin_amdgcn_sched_barrier(0)
; template <class Epi, class Sched, bool ALIGN_EPI = false, bool SP2 = false>
; __device__ __forceinline__ void gemm_phase(PG8_LAS unsigned char* lds, const Gemm g, const Sched& S, const Epi& E) {
;     ...
;             PG8_LDA(At, 1, 1); PG8_STAGE(PG8_SB(1, 0), b3, voffB); PG8_STAGE(PG8_SB(1, 1), b3 + hstepB, voffB); PG8_STAGE(PG8_SA(1, 0), a3, voffA);
;             PG8_WAIT_V(8); PG8_WAIT_L(0); PG8_BAR; PG8_MMA(1, 0, At, B0); PG8_MMA(1, 1, At, B1); PG8_BAR; PG8_SCHED;
	s_add_i32 s0, s33, s39
	v_lshl_add_u64 v[148:149], v[148:149], 0, s[22:23]
	s_mov_b32 m0, s0
	ds_read_b128 v[188:191], v154 offset:49152
	ds_read_b128 v[192:195], v154 offset:50176
	ds_read_b128 v[196:199], v154 offset:51200
	ds_read_b128 v[200:203], v154 offset:52224
	ds_read_b128 v[204:207], v154 offset:53248
	ds_read_b128 v[212:215], v154 offset:54272
	ds_read_b128 v[216:219], v154 offset:55296
	ds_read_b128 v[220:223], v154 offset:56320
	global_load_lds_dwordx4 v[148:149], off
	v_lshl_add_u64 v[148:149], v[208:209], 0, s[22:23]
	s_add_i32 m0, s0, 0x2000
	s_add_i32 s0, s63, s39
	global_load_lds_dwordx4 v[148:149], off
	v_lshl_add_u64 v[148:149], v[224:225], 0, s[22:23]
	s_mov_b32 m0, s0
	s_nop 0
	global_load_lds_dwordx4 v[148:149], off
	v_lshl_add_u64 v[148:149], v[226:227], 0, s[22:23]
	s_add_i32 m0, s0, 0x2000
	s_nop 0
	global_load_lds_dwordx4 v[148:149], off
	s_cmp_ge_i32 s61, s48
	s_cbranch_scc0 .Lkr4_b
	v_lshl_add_u64 v[148:149], v[228:229], 0, s[22:23]
	s_mov_b32 m0, s46
	s_nop 0
	global_load_lds_dwordx4 v[148:149], off
	v_lshl_add_u64 v[148:149], v[230:231], 0, s[22:23]
	s_mov_b32 m0, s47
	s_nop 0
	global_load_lds_dwordx4 v[148:149], off
.Lkr4_b:
	s_waitcnt vmcnt(6)
	s_waitcnt lgkmcnt(0)
	s_barrier
	s_setprio 1
	s_waitcnt lgkmcnt(0)
	v_mfma_f32_16x16x32_bf16 v[62:65], v[156:159], v[188:191], v[62:65]
	v_mfma_f32_16x16x32_bf16 v[58:61], v[164:167], v[188:191], v[58:61]
	v_mfma_f32_16x16x32_bf16 v[46:49], v[156:159], v[196:199], v[46:49]
	v_mfma_f32_16x16x32_bf16 v[42:45], v[164:167], v[196:199], v[42:45]
	v_mfma_f32_16x16x32_bf16 v[30:33], v[156:159], v[204:207], v[30:33]
	v_mfma_f32_16x16x32_bf16 v[26:29], v[164:167], v[204:207], v[26:29]
	v_mfma_f32_16x16x32_bf16 v[14:17], v[156:159], v[216:219], v[14:17]
	v_mfma_f32_16x16x32_bf16 v[6:9], v[164:167], v[216:219], v[6:9]
	v_mfma_f32_16x16x32_bf16 v[62:65], v[160:163], v[192:195], v[62:65]
	v_mfma_f32_16x16x32_bf16 v[58:61], v[168:171], v[192:195], v[58:61]
	v_mfma_f32_16x16x32_bf16 v[46:49], v[160:163], v[200:203], v[46:49]
	v_mfma_f32_16x16x32_bf16 v[42:45], v[168:171], v[200:203], v[42:45]
	v_mfma_f32_16x16x32_bf16 v[30:33], v[160:163], v[212:215], v[30:33]
	v_mfma_f32_16x16x32_bf16 v[26:29], v[168:171], v[212:215], v[26:29]
	v_mfma_f32_16x16x32_bf16 v[14:17], v[160:163], v[220:223], v[14:17]
	v_mfma_f32_16x16x32_bf16 v[6:9], v[168:171], v[220:223], v[6:9]
	s_setprio 0
	s_setprio 1
	v_mfma_f32_16x16x32_bf16 v[54:57], v[172:175], v[188:191], v[54:57]
	v_mfma_f32_16x16x32_bf16 v[50:53], v[180:183], v[188:191], v[50:53]
	v_mfma_f32_16x16x32_bf16 v[38:41], v[172:175], v[196:199], v[38:41]
	v_mfma_f32_16x16x32_bf16 v[34:37], v[180:183], v[196:199], v[34:37]
	v_mfma_f32_16x16x32_bf16 v[22:25], v[172:175], v[204:207], v[22:25]
	v_mfma_f32_16x16x32_bf16 v[18:21], v[180:183], v[204:207], v[18:21]
	v_mfma_f32_16x16x32_bf16 v[10:13], v[172:175], v[216:219], v[10:13]
	v_mfma_f32_16x16x32_bf16 v[2:5], v[180:183], v[216:219], v[2:5]
	v_mfma_f32_16x16x32_bf16 v[54:57], v[176:179], v[192:195], v[54:57]
	v_mfma_f32_16x16x32_bf16 v[50:53], v[184:187], v[192:195], v[50:53]
	v_mfma_f32_16x16x32_bf16 v[38:41], v[176:179], v[200:203], v[38:41]
	v_mfma_f32_16x16x32_bf16 v[34:37], v[184:187], v[200:203], v[34:37]
	v_mfma_f32_16x16x32_bf16 v[22:25], v[176:179], v[212:215], v[22:25]
	v_mfma_f32_16x16x32_bf16 v[18:21], v[184:187], v[212:215], v[18:21]
	v_mfma_f32_16x16x32_bf16 v[10:13], v[176:179], v[220:223], v[10:13]
	v_mfma_f32_16x16x32_bf16 v[2:5], v[184:187], v[220:223], v[2:5]
	s_setprio 0
	s_barrier
	s_add_u32 s30, s30, 0x100
	s_addc_u32 s31, s31, 0
	s_add_u32 s58, s58, 0x100
	s_addc_u32 s59, s59, 0
	s_cmp_ge_i32 s61, s48
	s_cselect_b32 s99, 0, 1
	s_mov_b32 s34, s61
	s_cbranch_scc0 .LBB0_1592

; #define PG8_STAGE(bufoff, gbase, voff) do { _Pragma("unroll") for (int _i = 0; _i < 2; ++_i) \
;         __builtin_amdgcn_global_load_lds((const unsigned*)((const char*)(gbase) + (voff)[_i]), (PG8_LAS unsigned*)(lds + (bufoff) + ldsw + _i * 8192), 16, 0, 0); } while (0)
; #define PG8_LDA(dst, b, h) do { _Pragma("unroll") for (int m = 0; m < 4; ++m) { const bf16x8 f0_ = *(const PG8_LAS bf16x8*)(lds + PG8_SA(b, h) + aoff + m * 2048), f1_ = *(const PG8_LAS bf16x8*)(lds + PG8_SA(b, h) + aoff + m * 2048 + 1024); dst[m].set(f0_, f1_); } } while (0)
; #define PG8_LDB(dst, b, h) do { _Pragma("unroll") for (int n = 0; n < 2; ++n) { const bf16x8 f0_ = *(const PG8_LAS bf16x8*)(lds + PG8_SB(b, h) + boff + n * 2048), f1_ = *(const PG8_LAS bf16x8*)(lds + PG8_SB(b, h) + boff + n * 2048 + 1024); dst[n].set(f0_, f1_); } } while (0)
; #define PG8_WAIT_V(n) asm volatile("s_waitcnt vmcnt(" #n ")" ::: "memory")
; #define PG8_WAIT_L(n) asm volatile("s_waitcnt lgkmcnt(" #n ")" ::: "memory")
; #define PG8_BAR __builtin_amdgcn_s_barrier()
; #define PG8_SCHED __builtin_amdgcn_sched_barrier(0)
; template <class Epi, class Sched, bool ALIGN_EPI = false, bool SP2 = false>
; __device__ __forceinline__ void gemm_phase(PG8_LAS unsigned char* lds, const Gemm g, const Sched& S, const Epi& E) {
;     ...
;             const bool last = (t == nt - 2);
;             const char* a1 = cA + (size_t)(t + 1) * kstep;
;             const char* a2 = last ? nA : cA + (size_t)(t + 2) * kstep; const char* b2 = last ? nB : cB + (size_t)(t + 2) * kstep;
;             const char* a3 = a2 + kstep; const char* b3 = b2 + kstep;
;             if (last && has_next) S.a_ready(nxt);
;             if constexpr (SP2) {
;             PG8_LDB(B0, 0, 0); PG8_LDB(B1, 0, 1); PG8_SCHED; PG8_LDA(At, 0, 0); PG8_STAGE(PG8_SA(1, 1), a1 + hstep, voffA);
;             PG8_WAIT_V(8); PG8_WAIT_L(0); PG8_BAR; PG8_MMA(0, 0, At, B0); PG8_MMA(0, 1, At, B1); PG8_BAR; PG8_SCHED;
;             PG8_LDA(At, 0, 1); PG8_STAGE(PG8_SB(0, 0), b2, voffB); PG8_STAGE(PG8_SB(0, 1), b2 + hstepB, voffB); PG8_STAGE(PG8_SA(0, 0), a2, voffA);
;             PG8_WAIT_V(8); PG8_WAIT_L(0); PG8_BAR; PG8_MMA(1, 0, At, B0); PG8_MMA(1, 1, At, B1); PG8_BAR; PG8_SCHED;
.LBB0_1625:
	ds_read_b128 v[18:21], v197
	ds_read_b128 v[22:25], v197 offset:1024
	ds_read_b128 v[26:29], v197 offset:2048
	ds_read_b128 v[30:33], v197 offset:3072
	ds_read_b128 v[2:5], v198
	ds_read_b128 v[6:9], v198 offset:1024
	ds_read_b128 v[10:13], v198 offset:2048
	ds_read_b128 v[14:17], v198 offset:3072
	s_add_i32 s82, s48, 2
	s_add_u32 s0, s46, 0x80
	s_addc_u32 s1, s47, 0
	s_cmp_eq_u32 s66, s48
	s_cselect_b32 s48, s2, s0
	s_cselect_b32 s49, s3, s1
	s_cselect_b32 s51, s45, s81
	s_cselect_b32 s50, s44, s80
	s_cmp_eq_u32 s99, 0
	s_cbranch_scc1 .Lkr5_a
	v_lshl_add_u64 v[192:193], v[192:193], 0, s[28:29]
	s_mov_b32 m0, s56
	v_lshl_add_u64 v[194:195], v[194:195], 0, s[28:29]
	global_load_lds_dwordx4 v[192:193], off
	s_mov_b32 m0, s57
	s_nop 0
	global_load_lds_dwordx4 v[194:195], off
.Lkr5_a:
	v_lshl_add_u64 v[192:193], s[46:47], 0, v[176:177]
	s_add_i32 m0, s10, 0xc000
	ds_read_b128 v[184:187], v199
	ds_read_b128 v[188:191], v199 offset:1024
	ds_read_b128 v[212:215], v199 offset:2048
	ds_read_b128 v[216:219], v199 offset:3072
	ds_read_b128 v[220:223], v199 offset:4096
	ds_read_b128 v[224:227], v199 offset:5120
	ds_read_b128 v[228:231], v199 offset:6144
	ds_read_b128 v[232:235], v199 offset:7168
	global_load_lds_dwordx4 v[192:193], off
	v_lshl_add_u64 v[192:193], s[46:47], 0, v[178:179]
	s_add_i32 m0, s10, 0xe000
	s_nop 0
	global_load_lds_dwordx4 v[192:193], off
	s_waitcnt vmcnt(8)
	s_waitcnt lgkmcnt(0)
	s_barrier
	s_setprio 1
	s_waitcnt lgkmcnt(0)
	v_mfma_scale_f32_16x16x128_f8f6f4 v[158:161], v[18:25], v[184:191], v[158:161], v200, v201 op_sel_hi:[0,0,0]
	v_mfma_scale_f32_16x16x128_f8f6f4 v[154:157], v[26:33], v[184:191], v[154:157], v200, v201 op_sel_hi:[0,0,0]
	v_mfma_scale_f32_16x16x128_f8f6f4 v[142:145], v[18:25], v[212:219], v[142:145], v200, v201 op_sel_hi:[0,0,0]
	v_mfma_scale_f32_16x16x128_f8f6f4 v[138:141], v[26:33], v[212:219], v[138:141], v200, v201 op_sel_hi:[0,0,0]
	v_mfma_scale_f32_16x16x128_f8f6f4 v[126:129], v[18:25], v[220:227], v[126:129], v200, v201 op_sel_hi:[0,0,0]
	v_mfma_scale_f32_16x16x128_f8f6f4 v[122:125], v[26:33], v[220:227], v[122:125], v200, v201 op_sel_hi:[0,0,0]
	v_mfma_scale_f32_16x16x128_f8f6f4 v[110:113], v[18:25], v[228:235], v[110:113], v200, v201 op_sel_hi:[0,0,0]
	v_mfma_scale_f32_16x16x128_f8f6f4 v[106:109], v[26:33], v[228:235], v[106:109], v200, v201 op_sel_hi:[0,0,0]
	s_setprio 0
	s_setprio 1
	v_mfma_scale_f32_16x16x128_f8f6f4 v[150:153], v[2:9], v[184:191], v[150:153], v200, v201 op_sel_hi:[0,0,0]
	v_mfma_scale_f32_16x16x128_f8f6f4 v[146:149], v[10:17], v[184:191], v[146:149], v200, v201 op_sel_hi:[0,0,0]
	v_mfma_scale_f32_16x16x128_f8f6f4 v[134:137], v[2:9], v[212:219], v[134:137], v200, v201 op_sel_hi:[0,0,0]
	v_mfma_scale_f32_16x16x128_f8f6f4 v[130:133], v[10:17], v[212:219], v[130:133], v200, v201 op_sel_hi:[0,0,0]
	v_mfma_scale_f32_16x16x128_f8f6f4 v[118:121], v[2:9], v[220:227], v[118:121], v200, v201 op_sel_hi:[0,0,0]
	v_mfma_scale_f32_16x16x128_f8f6f4 v[114:117], v[10:17], v[220:227], v[114:117], v200, v201 op_sel_hi:[0,0,0]
	v_mfma_scale_f32_16x16x128_f8f6f4 v[102:105], v[2:9], v[228:235], v[102:105], v200, v201 op_sel_hi:[0,0,0]
	v_mfma_scale_f32_16x16x128_f8f6f4 v[98:101], v[10:17], v[228:235], v[98:101], v200, v201 op_sel_hi:[0,0,0]
	s_setprio 0
	s_barrier
	s_add_i32 s0, s73, s9
	v_lshl_add_u64 v[184:185], s[50:51], 0, v[164:165]
	s_mov_b32 m0, s0
	ds_read_b128 v[212:215], v199 offset:16384
	ds_read_b128 v[216:219], v199 offset:17408
	ds_read_b128 v[220:223], v199 offset:18432
	ds_read_b128 v[224:227], v199 offset:19456
	ds_read_b128 v[228:231], v199 offset:20480
	ds_read_b128 v[232:235], v199 offset:21504
	ds_read_b128 v[236:239], v199 offset:22528
	ds_read_b128 v[240:243], v199 offset:23552
	global_load_lds_dwordx4 v[184:185], off
	s_add_i32 m0, s0, 0x2000
	s_add_u32 s0, s50, s14
	v_lshl_add_u64 v[186:187], s[50:51], 0, v[168:169]
	s_addc_u32 s1, s51, s15
	s_add_i32 s33, s74, s9
	global_load_lds_dwordx4 v[186:187], off
	v_lshl_add_u64 v[188:189], s[0:1], 0, v[164:165]
	s_mov_b32 m0, s33
	v_lshl_add_u64 v[190:191], s[0:1], 0, v[168:169]
	global_load_lds_dwordx4 v[188:189], off
	s_add_i32 m0, s33, 0x2000
	v_lshl_add_u64 v[192:193], s[48:49], 0, v[162:163]
	global_load_lds_dwordx4 v[190:191], off
	v_lshl_add_u64 v[194:195], s[48:49], 0, v[166:167]
	s_waitcnt vmcnt(6)
	s_waitcnt lgkmcnt(0)
	s_barrier
	s_setprio 1
	s_waitcnt lgkmcnt(0)
	v_mfma_scale_f32_16x16x128_f8f6f4 v[94:97], v[18:25], v[212:219], v[94:97], v200, v201 op_sel_hi:[0,0,0]
	v_mfma_scale_f32_16x16x128_f8f6f4 v[90:93], v[26:33], v[212:219], v[90:93], v200, v201 op_sel_hi:[0,0,0]
	v_mfma_scale_f32_16x16x128_f8f6f4 v[78:81], v[18:25], v[220:227], v[78:81], v200, v201 op_sel_hi:[0,0,0]
	v_mfma_scale_f32_16x16x128_f8f6f4 v[74:77], v[26:33], v[220:227], v[74:77], v200, v201 op_sel_hi:[0,0,0]
	v_mfma_scale_f32_16x16x128_f8f6f4 v[62:65], v[18:25], v[228:235], v[62:65], v200, v201 op_sel_hi:[0,0,0]
	v_mfma_scale_f32_16x16x128_f8f6f4 v[58:61], v[26:33], v[228:235], v[58:61], v200, v201 op_sel_hi:[0,0,0]
	v_mfma_scale_f32_16x16x128_f8f6f4 v[46:49], v[18:25], v[236:243], v[46:49], v200, v201 op_sel_hi:[0,0,0]
	v_mfma_scale_f32_16x16x128_f8f6f4 v[42:45], v[26:33], v[236:243], v[42:45], v200, v201 op_sel_hi:[0,0,0]
	s_setprio 0
	s_setprio 1
	v_mfma_scale_f32_16x16x128_f8f6f4 v[86:89], v[2:9], v[212:219], v[86:89], v200, v201 op_sel_hi:[0,0,0]
	v_mfma_scale_f32_16x16x128_f8f6f4 v[82:85], v[10:17], v[212:219], v[82:85], v200, v201 op_sel_hi:[0,0,0]
	v_mfma_scale_f32_16x16x128_f8f6f4 v[70:73], v[2:9], v[220:227], v[70:73], v200, v201 op_sel_hi:[0,0,0]
	v_mfma_scale_f32_16x16x128_f8f6f4 v[66:69], v[10:17], v[220:227], v[66:69], v200, v201 op_sel_hi:[0,0,0]
	v_mfma_scale_f32_16x16x128_f8f6f4 v[54:57], v[2:9], v[228:235], v[54:57], v200, v201 op_sel_hi:[0,0,0]
	v_mfma_scale_f32_16x16x128_f8f6f4 v[50:53], v[10:17], v[228:235], v[50:53], v200, v201 op_sel_hi:[0,0,0]
	v_mfma_scale_f32_16x16x128_f8f6f4 v[38:41], v[2:9], v[236:243], v[38:41], v200, v201 op_sel_hi:[0,0,0]
	v_mfma_scale_f32_16x16x128_f8f6f4 v[34:37], v[10:17], v[236:243], v[34:37], v200, v201 op_sel_hi:[0,0,0]
	s_setprio 0
	s_barrier
; #define PG8_STAGE(bufoff, gbase, voff) do { _Pragma("unroll") for (int _i = 0; _i < 2; ++_i) \
;         __builtin_amdgcn_global_load_lds((const unsigned*)((const char*)(gbase) + (voff)[_i]), (PG8_LAS unsigned*)(lds + (bufoff) + ldsw + _i * 8192), 16, 0, 0); } while (0)
; #define PG8_LDA(dst, b, h) do { _Pragma("unroll") for (int m = 0; m < 4; ++m) { const bf16x8 f0_ = *(const PG8_LAS bf16x8*)(lds + PG8_SA(b, h) + aoff + m * 2048), f1_ = *(const PG8_LAS bf16x8*)(lds + PG8_SA(b, h) + aoff + m * 2048 + 1024); dst[m].set(f0_, f1_); } } while (0)
; #define PG8_LDB(dst, b, h) do { _Pragma("unroll") for (int n = 0; n < 2; ++n) { const bf16x8 f0_ = *(const PG8_LAS bf16x8*)(lds + PG8_SB(b, h) + boff + n * 2048), f1_ = *(const PG8_LAS bf16x8*)(lds + PG8_SB(b, h) + boff + n * 2048 + 1024); dst[n].set(f0_, f1_); } } while (0)
; #define PG8_WAIT_V(n) asm volatile("s_waitcnt vmcnt(" #n ")" ::: "memory")
; #define PG8_WAIT_L(n) asm volatile("s_waitcnt lgkmcnt(" #n ")" ::: "memory")
; #define PG8_BAR __builtin_amdgcn_s_barrier()
; #define PG8_SCHED __builtin_amdgcn_sched_barrier(0)
; template <class Epi, class Sched, bool ALIGN_EPI = false, bool SP2 = false>
; __device__ __forceinline__ void gemm_phase(PG8_LAS unsigned char* lds, const Gemm g, const Sched& S, const Epi& E) {
;     ...
;         for (int t = 0; t < nt; t += 2) {
;     ...
;             PG8_LDB(B0, 1, 0); PG8_LDB(B1, 1, 1); PG8_SCHED; PG8_LDA(At, 1, 0); PG8_STAGE(PG8_SA(0, 1), a2 + hstep, voffA);
;             PG8_WAIT_V(8); PG8_WAIT_L(0); PG8_BAR; PG8_MMA(0, 0, At, B0); PG8_MMA(0, 1, At, B1); PG8_BAR; PG8_SCHED;
;             PG8_LDA(At, 1, 1); PG8_STAGE(PG8_SB(1, 0), b3, voffB); PG8_STAGE(PG8_SB(1, 1), b3 + hstepB, voffB); PG8_STAGE(PG8_SA(1, 0), a3, voffA);
;             PG8_WAIT_V(8); PG8_WAIT_L(0); PG8_BAR; PG8_MMA(1, 0, At, B0); PG8_MMA(1, 1, At, B1); PG8_BAR; PG8_SCHED;
	s_add_i32 s33, 0, 0x18000
	s_add_i32 s50, 0, 0x1c000
	v_add_u32_e32 v14, s33, v173
	v_add_u32_e32 v30, s50, v173
	ds_read_b128 v[2:5], v14
	ds_read_b128 v[6:9], v14 offset:1024
	ds_read_b128 v[10:13], v14 offset:2048
	ds_read_b128 v[14:17], v14 offset:3072
	ds_read_b128 v[18:21], v30
	ds_read_b128 v[22:25], v30 offset:1024
	ds_read_b128 v[26:29], v30 offset:2048
	ds_read_b128 v[30:33], v30 offset:3072
	s_add_u32 s0, s48, s12
	s_addc_u32 s1, s49, s13
	s_mov_b32 m0, s52
	v_lshl_add_u64 v[204:205], s[0:1], 0, v[162:163]
	ds_read_b128 v[212:215], v199 offset:32768
	ds_read_b128 v[216:219], v199 offset:33792
	ds_read_b128 v[220:223], v199 offset:34816
	ds_read_b128 v[224:227], v199 offset:35840
	ds_read_b128 v[228:231], v199 offset:36864
	ds_read_b128 v[232:235], v199 offset:37888
	ds_read_b128 v[236:239], v199 offset:38912
	ds_read_b128 v[240:243], v199 offset:39936
	s_mov_b32 m0, s10
	s_nop 0
	global_load_lds_dwordx4 v[192:193], off
	s_mov_b32 m0, s11
	s_nop 0
	global_load_lds_dwordx4 v[194:195], off
	s_mov_b32 m0, s52
	s_nop 0
	global_load_lds_dwordx4 v[204:205], off
	v_lshl_add_u64 v[204:205], s[0:1], 0, v[166:167]
	s_mov_b32 m0, s53
	s_nop 0
	global_load_lds_dwordx4 v[204:205], off
	s_waitcnt vmcnt(8)
	s_waitcnt lgkmcnt(0)
	s_barrier
	s_setprio 1
	s_waitcnt lgkmcnt(0)
	v_mfma_scale_f32_16x16x128_f8f6f4 v[158:161], v[2:9], v[212:219], v[158:161], v200, v201 op_sel_hi:[0,0,0]
	v_mfma_scale_f32_16x16x128_f8f6f4 v[154:157], v[10:17], v[212:219], v[154:157], v200, v201 op_sel_hi:[0,0,0]
	v_mfma_scale_f32_16x16x128_f8f6f4 v[142:145], v[2:9], v[220:227], v[142:145], v200, v201 op_sel_hi:[0,0,0]
	v_mfma_scale_f32_16x16x128_f8f6f4 v[138:141], v[10:17], v[220:227], v[138:141], v200, v201 op_sel_hi:[0,0,0]
	v_mfma_scale_f32_16x16x128_f8f6f4 v[126:129], v[2:9], v[228:235], v[126:129], v200, v201 op_sel_hi:[0,0,0]
	v_mfma_scale_f32_16x16x128_f8f6f4 v[122:125], v[10:17], v[228:235], v[122:125], v200, v201 op_sel_hi:[0,0,0]
	v_mfma_scale_f32_16x16x128_f8f6f4 v[110:113], v[2:9], v[236:243], v[110:113], v200, v201 op_sel_hi:[0,0,0]
	v_mfma_scale_f32_16x16x128_f8f6f4 v[106:109], v[10:17], v[236:243], v[106:109], v200, v201 op_sel_hi:[0,0,0]
	s_setprio 0
	s_setprio 1
	v_mfma_scale_f32_16x16x128_f8f6f4 v[150:153], v[18:25], v[212:219], v[150:153], v200, v201 op_sel_hi:[0,0,0]
	v_mfma_scale_f32_16x16x128_f8f6f4 v[146:149], v[26:33], v[212:219], v[146:149], v200, v201 op_sel_hi:[0,0,0]
	v_mfma_scale_f32_16x16x128_f8f6f4 v[134:137], v[18:25], v[220:227], v[134:137], v200, v201 op_sel_hi:[0,0,0]
	v_mfma_scale_f32_16x16x128_f8f6f4 v[130:133], v[26:33], v[220:227], v[130:133], v200, v201 op_sel_hi:[0,0,0]
	v_mfma_scale_f32_16x16x128_f8f6f4 v[118:121], v[18:25], v[228:235], v[118:121], v200, v201 op_sel_hi:[0,0,0]
	v_mfma_scale_f32_16x16x128_f8f6f4 v[114:117], v[26:33], v[228:235], v[114:117], v200, v201 op_sel_hi:[0,0,0]
	v_mfma_scale_f32_16x16x128_f8f6f4 v[102:105], v[18:25], v[236:243], v[102:105], v200, v201 op_sel_hi:[0,0,0]
	v_mfma_scale_f32_16x16x128_f8f6f4 v[98:101], v[26:33], v[236:243], v[98:101], v200, v201 op_sel_hi:[0,0,0]
	s_setprio 0
	s_barrier
	s_add_i32 s0, s33, s9
	v_lshl_add_u64 v[184:185], v[184:185], 0, s[28:29]
	s_mov_b32 m0, s0
	ds_read_b128 v[212:215], v199 offset:49152
	ds_read_b128 v[216:219], v199 offset:50176
	ds_read_b128 v[220:223], v199 offset:51200
	ds_read_b128 v[224:227], v199 offset:52224
	ds_read_b128 v[228:231], v199 offset:53248
	ds_read_b128 v[232:235], v199 offset:54272
	ds_read_b128 v[236:239], v199 offset:55296
	ds_read_b128 v[240:243], v199 offset:56320
	global_load_lds_dwordx4 v[184:185], off
	v_lshl_add_u64 v[184:185], v[186:187], 0, s[28:29]
	s_add_i32 m0, s0, 0x2000
	s_add_i32 s0, s50, s9
	global_load_lds_dwordx4 v[184:185], off
	v_lshl_add_u64 v[184:185], v[188:189], 0, s[28:29]
	s_mov_b32 m0, s0
	s_nop 0
	global_load_lds_dwordx4 v[184:185], off
	v_lshl_add_u64 v[184:185], v[190:191], 0, s[28:29]
	s_add_i32 m0, s0, 0x2000
	s_nop 0
	global_load_lds_dwordx4 v[184:185], off
	s_cmp_ge_i32 s82, s58
	s_cbranch_scc0 .Lkr5_b
	v_lshl_add_u64 v[184:185], v[192:193], 0, s[28:29]
	s_mov_b32 m0, s56
	s_nop 0
	global_load_lds_dwordx4 v[184:185], off
	v_lshl_add_u64 v[184:185], v[194:195], 0, s[28:29]
	s_mov_b32 m0, s57
	s_nop 0
	global_load_lds_dwordx4 v[184:185], off
.Lkr5_b:
	s_waitcnt vmcnt(6)
	s_waitcnt lgkmcnt(0)
	s_barrier
	s_setprio 1
	s_waitcnt lgkmcnt(0)
	v_mfma_scale_f32_16x16x128_f8f6f4 v[94:97], v[2:9], v[212:219], v[94:97], v200, v201 op_sel_hi:[0,0,0]
	v_mfma_scale_f32_16x16x128_f8f6f4 v[90:93], v[10:17], v[212:219], v[90:93], v200, v201 op_sel_hi:[0,0,0]
	v_mfma_scale_f32_16x16x128_f8f6f4 v[78:81], v[2:9], v[220:227], v[78:81], v200, v201 op_sel_hi:[0,0,0]
	v_mfma_scale_f32_16x16x128_f8f6f4 v[74:77], v[10:17], v[220:227], v[74:77], v200, v201 op_sel_hi:[0,0,0]
	v_mfma_scale_f32_16x16x128_f8f6f4 v[62:65], v[2:9], v[228:235], v[62:65], v200, v201 op_sel_hi:[0,0,0]
	v_mfma_scale_f32_16x16x128_f8f6f4 v[58:61], v[10:17], v[228:235], v[58:61], v200, v201 op_sel_hi:[0,0,0]
	v_mfma_scale_f32_16x16x128_f8f6f4 v[46:49], v[2:9], v[236:243], v[46:49], v200, v201 op_sel_hi:[0,0,0]
	v_mfma_scale_f32_16x16x128_f8f6f4 v[42:45], v[10:17], v[236:243], v[42:45], v200, v201 op_sel_hi:[0,0,0]
	s_setprio 0
	s_setprio 1
	v_mfma_scale_f32_16x16x128_f8f6f4 v[86:89], v[18:25], v[212:219], v[86:89], v200, v201 op_sel_hi:[0,0,0]
	v_mfma_scale_f32_16x16x128_f8f6f4 v[82:85], v[26:33], v[212:219], v[82:85], v200, v201 op_sel_hi:[0,0,0]
	v_mfma_scale_f32_16x16x128_f8f6f4 v[70:73], v[18:25], v[220:227], v[70:73], v200, v201 op_sel_hi:[0,0,0]
	v_mfma_scale_f32_16x16x128_f8f6f4 v[66:69], v[26:33], v[220:227], v[66:69], v200, v201 op_sel_hi:[0,0,0]
	v_mfma_scale_f32_16x16x128_f8f6f4 v[54:57], v[18:25], v[228:235], v[54:57], v200, v201 op_sel_hi:[0,0,0]
	v_mfma_scale_f32_16x16x128_f8f6f4 v[50:53], v[26:33], v[228:235], v[50:53], v200, v201 op_sel_hi:[0,0,0]
	v_mfma_scale_f32_16x16x128_f8f6f4 v[38:41], v[18:25], v[236:243], v[38:41], v200, v201 op_sel_hi:[0,0,0]
	v_mfma_scale_f32_16x16x128_f8f6f4 v[34:37], v[26:33], v[236:243], v[34:37], v200, v201 op_sel_hi:[0,0,0]
	s_setprio 0
	s_barrier
	s_add_u32 s46, s46, 0x100
	s_addc_u32 s47, s47, 0
	s_add_u32 s80, s80, 0x100
	s_addc_u32 s81, s81, 0
	s_cmp_ge_i32 s82, s58
	s_cselect_b32 s99, 0, 1
	s_mov_b32 s48, s82
	s_cbranch_scc0 .LBB0_1625

; #define PG8_STAGE(bufoff, gbase, voff) do { _Pragma("unroll") for (int _i = 0; _i < 2; ++_i) \
;         __builtin_amdgcn_global_load_lds((const unsigned*)((const char*)(gbase) + (voff)[_i]), (PG8_LAS unsigned*)(lds + (bufoff) + ldsw + _i * 8192), 16, 0, 0); } while (0)
; #define PG8_LDA(dst, b, h) do { _Pragma("unroll") for (int m = 0; m < 4; ++m) { const bf16x8 f0_ = *(const PG8_LAS bf16x8*)(lds + PG8_SA(b, h) + aoff + m * 2048), f1_ = *(const PG8_LAS bf16x8*)(lds + PG8_SA(b, h) + aoff + m * 2048 + 1024); dst[m].set(f0_, f1_); } } while (0)
; #define PG8_LDB(dst, b, h) do { _Pragma("unroll") for (int n = 0; n < 2; ++n) { const bf16x8 f0_ = *(const PG8_LAS bf16x8*)(lds + PG8_SB(b, h) + boff + n * 2048), f1_ = *(const PG8_LAS bf16x8*)(lds + PG8_SB(b, h) + boff + n * 2048 + 1024); dst[n].set(f0_, f1_); } } while (0)
; #define PG8_WAIT_V(n) asm volatile("s_waitcnt vmcnt(" #n ")" ::: "memory")
; #define PG8_WAIT_L(n) asm volatile("s_waitcnt lgkmcnt(" #n ")" ::: "memory")
; #define PG8_BAR __builtin_amdgcn_s_barrier()
; #define PG8_SCHED __builtin_amdgcn_sched_barrier(0)
; template <class Epi, class Sched, bool ALIGN_EPI = false, bool SP2 = false>
; __device__ __forceinline__ void gemm_phase(PG8_LAS unsigned char* lds, const Gemm g, const Sched& S, const Epi& E) {
;     ...
;             const bool last = (t == nt - 2);
;             const char* a1 = cA + (size_t)(t + 1) * kstep;
;             const char* a2 = last ? nA : cA + (size_t)(t + 2) * kstep; const char* b2 = last ? nB : cB + (size_t)(t + 2) * kstep;
;             const char* a3 = a2 + kstep; const char* b3 = b2 + kstep;
;             if (last && has_next) S.a_ready(nxt);
;             if constexpr (SP2) {
;             PG8_LDB(B0, 0, 0); PG8_LDB(B1, 0, 1); PG8_SCHED; PG8_LDA(At, 0, 0); PG8_STAGE(PG8_SA(1, 1), a1 + hstep, voffA);
;             PG8_WAIT_V(8); PG8_WAIT_L(0); PG8_BAR; PG8_MMA(0, 0, At, B0); PG8_MMA(0, 1, At, B1); PG8_BAR; PG8_SCHED;
;             PG8_LDA(At, 0, 1); PG8_STAGE(PG8_SB(0, 0), b2, voffB); PG8_STAGE(PG8_SB(0, 1), b2 + hstepB, voffB); PG8_STAGE(PG8_SA(0, 0), a2, voffA);
;             PG8_WAIT_V(8); PG8_WAIT_L(0); PG8_BAR; PG8_MMA(1, 0, At, B0); PG8_MMA(1, 1, At, B1); PG8_BAR; PG8_SCHED;
.LBB0_1658:
	ds_read_b128 v[16:19], v215
	ds_read_b128 v[20:23], v215 offset:1024
	ds_read_b128 v[24:27], v215 offset:2048
	ds_read_b128 v[28:31], v215 offset:3072
	ds_read_b128 v[0:3], v216
	ds_read_b128 v[4:7], v216 offset:1024
	ds_read_b128 v[8:11], v216 offset:2048
	ds_read_b128 v[12:15], v216 offset:3072
	s_add_i32 s83, s78, 2
	s_add_u32 s0, s2, 0x80
	s_addc_u32 s1, s3, 0
	s_cmp_eq_u32 s97, s78
	s_cselect_b32 s78, s58, s0
	s_cselect_b32 s79, s59, s1
	s_cselect_b32 s81, s75, s82
	s_cselect_b32 s80, s74, s57
	s_cmp_eq_u32 s99, 0
	s_cbranch_scc1 .Lkr6_a
	v_lshl_add_u64 v[168:169], v[168:169], 0, s[36:37]
	s_mov_b32 m0, s93
	v_lshl_add_u64 v[170:171], v[170:171], 0, s[36:37]
	global_load_lds_dwordx4 v[168:169], off
	s_mov_b32 m0, s94
	s_nop 0
	global_load_lds_dwordx4 v[170:171], off
.Lkr6_a:
	v_lshl_add_u64 v[206:207], s[2:3], 0, v[198:199]
	s_add_i32 m0, s71, 0xc000
	ds_read_b128 v[152:155], v217
	ds_read_b128 v[156:159], v217 offset:1024
	ds_read_b128 v[168:171], v217 offset:2048
	ds_read_b128 v[172:175], v217 offset:3072
	ds_read_b128 v[176:179], v217 offset:4096
	ds_read_b128 v[180:183], v217 offset:5120
	ds_read_b128 v[226:229], v217 offset:6144
	ds_read_b128 v[230:233], v217 offset:7168
	global_load_lds_dwordx4 v[206:207], off
	v_lshl_add_u64 v[206:207], s[2:3], 0, v[200:201]
	s_add_i32 m0, s71, 0xe000
	s_nop 0
	global_load_lds_dwordx4 v[206:207], off
	s_waitcnt vmcnt(8)
	s_waitcnt lgkmcnt(0)
	s_barrier
	s_setprio 1
	s_waitcnt lgkmcnt(0)
	v_mfma_scale_f32_16x16x128_f8f6f4 v[164:167], v[16:23], v[152:159], v[164:167], v218, v219 op_sel_hi:[0,0,0]
	v_mfma_scale_f32_16x16x128_f8f6f4 v[160:163], v[24:31], v[152:159], v[160:163], v218, v219 op_sel_hi:[0,0,0]
	v_mfma_scale_f32_16x16x128_f8f6f4 v[140:143], v[16:23], v[168:175], v[140:143], v218, v219 op_sel_hi:[0,0,0]
	v_mfma_scale_f32_16x16x128_f8f6f4 v[136:139], v[24:31], v[168:175], v[136:139], v218, v219 op_sel_hi:[0,0,0]
	v_mfma_scale_f32_16x16x128_f8f6f4 v[108:111], v[16:23], v[176:183], v[108:111], v218, v219 op_sel_hi:[0,0,0]
	v_mfma_scale_f32_16x16x128_f8f6f4 v[104:107], v[24:31], v[176:183], v[104:107], v218, v219 op_sel_hi:[0,0,0]
	v_mfma_scale_f32_16x16x128_f8f6f4 v[116:119], v[16:23], v[226:233], v[116:119], v218, v219 op_sel_hi:[0,0,0]
	v_mfma_scale_f32_16x16x128_f8f6f4 v[112:115], v[24:31], v[226:233], v[112:115], v218, v219 op_sel_hi:[0,0,0]
	s_setprio 0
	s_setprio 1
	v_mfma_scale_f32_16x16x128_f8f6f4 v[148:151], v[0:7], v[152:159], v[148:151], v218, v219 op_sel_hi:[0,0,0]
	v_mfma_scale_f32_16x16x128_f8f6f4 v[144:147], v[8:15], v[152:159], v[144:147], v218, v219 op_sel_hi:[0,0,0]
	v_mfma_scale_f32_16x16x128_f8f6f4 v[132:135], v[0:7], v[168:175], v[132:135], v218, v219 op_sel_hi:[0,0,0]
	v_mfma_scale_f32_16x16x128_f8f6f4 v[128:131], v[8:15], v[168:175], v[128:131], v218, v219 op_sel_hi:[0,0,0]
	v_mfma_scale_f32_16x16x128_f8f6f4 v[124:127], v[0:7], v[176:183], v[124:127], v218, v219 op_sel_hi:[0,0,0]
	v_mfma_scale_f32_16x16x128_f8f6f4 v[120:123], v[8:15], v[176:183], v[120:123], v218, v219 op_sel_hi:[0,0,0]
	v_mfma_scale_f32_16x16x128_f8f6f4 v[100:103], v[0:7], v[226:233], v[100:103], v218, v219 op_sel_hi:[0,0,0]
	v_mfma_scale_f32_16x16x128_f8f6f4 v[96:99], v[8:15], v[226:233], v[96:99], v218, v219 op_sel_hi:[0,0,0]
	s_setprio 0
	s_barrier
	s_add_i32 s0, s67, s45
	v_lshl_add_u64 v[152:153], s[80:81], 0, v[186:187]
	s_mov_b32 m0, s0
	ds_read_b128 v[172:175], v217 offset:16384
	ds_read_b128 v[176:179], v217 offset:17408
	ds_read_b128 v[226:229], v217 offset:18432
	ds_read_b128 v[230:233], v217 offset:19456
	ds_read_b128 v[234:237], v217 offset:20480
	ds_read_b128 v[238:241], v217 offset:21504
	ds_read_b128 v[242:245], v217 offset:22528
	ds_read_b128 v[246:249], v217 offset:23552
	global_load_lds_dwordx4 v[152:153], off
	s_add_i32 m0, s0, 0x2000
	s_add_u32 s0, s80, s20
	v_lshl_add_u64 v[154:155], s[80:81], 0, v[190:191]
	s_addc_u32 s1, s81, s21
	s_add_i32 s33, s10, s45
	global_load_lds_dwordx4 v[154:155], off
	v_lshl_add_u64 v[156:157], s[0:1], 0, v[186:187]
	s_mov_b32 m0, s33
	v_lshl_add_u64 v[158:159], s[0:1], 0, v[190:191]
	global_load_lds_dwordx4 v[156:157], off
	s_add_i32 m0, s33, 0x2000
	v_lshl_add_u64 v[168:169], s[78:79], 0, v[184:185]
	global_load_lds_dwordx4 v[158:159], off
	v_lshl_add_u64 v[170:171], s[78:79], 0, v[188:189]
	s_waitcnt vmcnt(6)
	s_waitcnt lgkmcnt(0)
	s_barrier
	s_setprio 1
	s_waitcnt lgkmcnt(0)
	v_mfma_scale_f32_16x16x128_f8f6f4 v[92:95], v[16:23], v[172:179], v[92:95], v218, v219 op_sel_hi:[0,0,0]
	v_mfma_scale_f32_16x16x128_f8f6f4 v[88:91], v[24:31], v[172:179], v[88:91], v218, v219 op_sel_hi:[0,0,0]
	v_mfma_scale_f32_16x16x128_f8f6f4 v[76:79], v[16:23], v[226:233], v[76:79], v218, v219 op_sel_hi:[0,0,0]
	v_mfma_scale_f32_16x16x128_f8f6f4 v[72:75], v[24:31], v[226:233], v[72:75], v218, v219 op_sel_hi:[0,0,0]
	v_mfma_scale_f32_16x16x128_f8f6f4 v[60:63], v[16:23], v[234:241], v[60:63], v218, v219 op_sel_hi:[0,0,0]
	v_mfma_scale_f32_16x16x128_f8f6f4 v[56:59], v[24:31], v[234:241], v[56:59], v218, v219 op_sel_hi:[0,0,0]
	v_mfma_scale_f32_16x16x128_f8f6f4 v[44:47], v[16:23], v[242:249], v[44:47], v218, v219 op_sel_hi:[0,0,0]
	v_mfma_scale_f32_16x16x128_f8f6f4 v[40:43], v[24:31], v[242:249], v[40:43], v218, v219 op_sel_hi:[0,0,0]
	s_setprio 0
	s_setprio 1
	v_mfma_scale_f32_16x16x128_f8f6f4 v[84:87], v[0:7], v[172:179], v[84:87], v218, v219 op_sel_hi:[0,0,0]
	v_mfma_scale_f32_16x16x128_f8f6f4 v[80:83], v[8:15], v[172:179], v[80:83], v218, v219 op_sel_hi:[0,0,0]
	v_mfma_scale_f32_16x16x128_f8f6f4 v[68:71], v[0:7], v[226:233], v[68:71], v218, v219 op_sel_hi:[0,0,0]
	v_mfma_scale_f32_16x16x128_f8f6f4 v[64:67], v[8:15], v[226:233], v[64:67], v218, v219 op_sel_hi:[0,0,0]
	v_mfma_scale_f32_16x16x128_f8f6f4 v[52:55], v[0:7], v[234:241], v[52:55], v218, v219 op_sel_hi:[0,0,0]
	v_mfma_scale_f32_16x16x128_f8f6f4 v[48:51], v[8:15], v[234:241], v[48:51], v218, v219 op_sel_hi:[0,0,0]
	v_mfma_scale_f32_16x16x128_f8f6f4 v[36:39], v[0:7], v[242:249], v[36:39], v218, v219 op_sel_hi:[0,0,0]
	v_mfma_scale_f32_16x16x128_f8f6f4 v[32:35], v[8:15], v[242:249], v[32:35], v218, v219 op_sel_hi:[0,0,0]
	s_setprio 0
	s_barrier
; #define PG8_STAGE(bufoff, gbase, voff) do { _Pragma("unroll") for (int _i = 0; _i < 2; ++_i) \
;         __builtin_amdgcn_global_load_lds((const unsigned*)((const char*)(gbase) + (voff)[_i]), (PG8_LAS unsigned*)(lds + (bufoff) + ldsw + _i * 8192), 16, 0, 0); } while (0)
; #define PG8_LDA(dst, b, h) do { _Pragma("unroll") for (int m = 0; m < 4; ++m) { const bf16x8 f0_ = *(const PG8_LAS bf16x8*)(lds + PG8_SA(b, h) + aoff + m * 2048), f1_ = *(const PG8_LAS bf16x8*)(lds + PG8_SA(b, h) + aoff + m * 2048 + 1024); dst[m].set(f0_, f1_); } } while (0)
; #define PG8_LDB(dst, b, h) do { _Pragma("unroll") for (int n = 0; n < 2; ++n) { const bf16x8 f0_ = *(const PG8_LAS bf16x8*)(lds + PG8_SB(b, h) + boff + n * 2048), f1_ = *(const PG8_LAS bf16x8*)(lds + PG8_SB(b, h) + boff + n * 2048 + 1024); dst[n].set(f0_, f1_); } } while (0)
; #define PG8_WAIT_V(n) asm volatile("s_waitcnt vmcnt(" #n ")" ::: "memory")
; #define PG8_WAIT_L(n) asm volatile("s_waitcnt lgkmcnt(" #n ")" ::: "memory")
; #define PG8_BAR __builtin_amdgcn_s_barrier()
; #define PG8_SCHED __builtin_amdgcn_sched_barrier(0)
; template <class Epi, class Sched, bool ALIGN_EPI = false, bool SP2 = false>
; __device__ __forceinline__ void gemm_phase(PG8_LAS unsigned char* lds, const Gemm g, const Sched& S, const Epi& E) {
;     ...
;         for (int t = 0; t < nt; t += 2) {
;     ...
;             PG8_LDB(B0, 1, 0); PG8_LDB(B1, 1, 1); PG8_SCHED; PG8_LDA(At, 1, 0); PG8_STAGE(PG8_SA(0, 1), a2 + hstep, voffA);
;             PG8_WAIT_V(8); PG8_WAIT_L(0); PG8_BAR; PG8_MMA(0, 0, At, B0); PG8_MMA(0, 1, At, B1); PG8_BAR; PG8_SCHED;
;             PG8_LDA(At, 1, 1); PG8_STAGE(PG8_SB(1, 0), b3, voffB); PG8_STAGE(PG8_SB(1, 1), b3 + hstepB, voffB); PG8_STAGE(PG8_SA(1, 0), a3, voffA);
;             PG8_WAIT_V(8); PG8_WAIT_L(0); PG8_BAR; PG8_MMA(1, 0, At, B0); PG8_MMA(1, 1, At, B1); PG8_BAR; PG8_SCHED;
	s_add_i32 s33, 0, 0x18000
	s_add_i32 s80, 0, 0x1c000
	v_add_u32_e32 v12, s33, v211
	v_add_u32_e32 v28, s80, v211
	ds_read_b128 v[0:3], v12
	ds_read_b128 v[4:7], v12 offset:1024
	ds_read_b128 v[8:11], v12 offset:2048
	ds_read_b128 v[12:15], v12 offset:3072
	ds_read_b128 v[16:19], v28
	ds_read_b128 v[20:23], v28 offset:1024
	ds_read_b128 v[24:27], v28 offset:2048
	ds_read_b128 v[28:31], v28 offset:3072
	s_add_u32 s0, s78, s18
	s_addc_u32 s1, s79, s19
	s_mov_b32 m0, s86
	v_lshl_add_u64 v[180:181], s[0:1], 0, v[184:185]
	ds_read_b128 v[172:175], v217 offset:32768
	ds_read_b128 v[176:179], v217 offset:33792
	ds_read_b128 v[226:229], v217 offset:34816
	ds_read_b128 v[230:233], v217 offset:35840
	ds_read_b128 v[234:237], v217 offset:36864
	ds_read_b128 v[238:241], v217 offset:37888
	ds_read_b128 v[242:245], v217 offset:38912
	ds_read_b128 v[246:249], v217 offset:39936
	s_mov_b32 m0, s71
	s_nop 0
	global_load_lds_dwordx4 v[168:169], off
	s_mov_b32 m0, s73
	s_nop 0
	global_load_lds_dwordx4 v[170:171], off
	s_mov_b32 m0, s86
	s_nop 0
	global_load_lds_dwordx4 v[180:181], off
	v_lshl_add_u64 v[180:181], s[0:1], 0, v[188:189]
	s_mov_b32 m0, s87
	s_nop 0
	global_load_lds_dwordx4 v[180:181], off
	s_waitcnt vmcnt(8)
	s_waitcnt lgkmcnt(0)
	s_barrier
	s_setprio 1
	s_waitcnt lgkmcnt(0)
	v_mfma_scale_f32_16x16x128_f8f6f4 v[164:167], v[0:7], v[172:179], v[164:167], v218, v219 op_sel_hi:[0,0,0]
	v_mfma_scale_f32_16x16x128_f8f6f4 v[160:163], v[8:15], v[172:179], v[160:163], v218, v219 op_sel_hi:[0,0,0]
	v_mfma_scale_f32_16x16x128_f8f6f4 v[140:143], v[0:7], v[226:233], v[140:143], v218, v219 op_sel_hi:[0,0,0]
	v_mfma_scale_f32_16x16x128_f8f6f4 v[136:139], v[8:15], v[226:233], v[136:139], v218, v219 op_sel_hi:[0,0,0]
	v_mfma_scale_f32_16x16x128_f8f6f4 v[108:111], v[0:7], v[234:241], v[108:111], v218, v219 op_sel_hi:[0,0,0]
	v_mfma_scale_f32_16x16x128_f8f6f4 v[104:107], v[8:15], v[234:241], v[104:107], v218, v219 op_sel_hi:[0,0,0]
	v_mfma_scale_f32_16x16x128_f8f6f4 v[116:119], v[0:7], v[242:249], v[116:119], v218, v219 op_sel_hi:[0,0,0]
	v_mfma_scale_f32_16x16x128_f8f6f4 v[112:115], v[8:15], v[242:249], v[112:115], v218, v219 op_sel_hi:[0,0,0]
	s_setprio 0
	s_setprio 1
	v_mfma_scale_f32_16x16x128_f8f6f4 v[148:151], v[16:23], v[172:179], v[148:151], v218, v219 op_sel_hi:[0,0,0]
	v_mfma_scale_f32_16x16x128_f8f6f4 v[144:147], v[24:31], v[172:179], v[144:147], v218, v219 op_sel_hi:[0,0,0]
	v_mfma_scale_f32_16x16x128_f8f6f4 v[132:135], v[16:23], v[226:233], v[132:135], v218, v219 op_sel_hi:[0,0,0]
	v_mfma_scale_f32_16x16x128_f8f6f4 v[128:131], v[24:31], v[226:233], v[128:131], v218, v219 op_sel_hi:[0,0,0]
	v_mfma_scale_f32_16x16x128_f8f6f4 v[124:127], v[16:23], v[234:241], v[124:127], v218, v219 op_sel_hi:[0,0,0]
	v_mfma_scale_f32_16x16x128_f8f6f4 v[120:123], v[24:31], v[234:241], v[120:123], v218, v219 op_sel_hi:[0,0,0]
	v_mfma_scale_f32_16x16x128_f8f6f4 v[100:103], v[16:23], v[242:249], v[100:103], v218, v219 op_sel_hi:[0,0,0]
	v_mfma_scale_f32_16x16x128_f8f6f4 v[96:99], v[24:31], v[242:249], v[96:99], v218, v219 op_sel_hi:[0,0,0]
	s_setprio 0
	s_barrier
	s_add_i32 s0, s33, s45
	v_lshl_add_u64 v[152:153], v[152:153], 0, s[36:37]
	s_mov_b32 m0, s0
	ds_read_b128 v[172:175], v217 offset:49152
	ds_read_b128 v[176:179], v217 offset:50176
	ds_read_b128 v[226:229], v217 offset:51200
	ds_read_b128 v[230:233], v217 offset:52224
	ds_read_b128 v[234:237], v217 offset:53248
	ds_read_b128 v[238:241], v217 offset:54272
	ds_read_b128 v[242:245], v217 offset:55296
	ds_read_b128 v[246:249], v217 offset:56320
	global_load_lds_dwordx4 v[152:153], off
	v_lshl_add_u64 v[152:153], v[154:155], 0, s[36:37]
	s_add_i32 m0, s0, 0x2000
	s_add_i32 s0, s80, s45
	global_load_lds_dwordx4 v[152:153], off
	v_lshl_add_u64 v[152:153], v[156:157], 0, s[36:37]
	s_mov_b32 m0, s0
	s_nop 0
	global_load_lds_dwordx4 v[152:153], off
	v_lshl_add_u64 v[152:153], v[158:159], 0, s[36:37]
	s_add_i32 m0, s0, 0x2000
	s_nop 0
	global_load_lds_dwordx4 v[152:153], off
	s_cmp_ge_i32 s83, s91
	s_cbranch_scc0 .Lkr6_b
	v_lshl_add_u64 v[152:153], v[168:169], 0, s[36:37]
	s_mov_b32 m0, s93
	s_nop 0
	global_load_lds_dwordx4 v[152:153], off
	v_lshl_add_u64 v[152:153], v[170:171], 0, s[36:37]
	s_mov_b32 m0, s94
	s_nop 0
	global_load_lds_dwordx4 v[152:153], off
.Lkr6_b:
	s_waitcnt vmcnt(6)
	s_waitcnt lgkmcnt(0)
	s_barrier
	s_setprio 1
	s_waitcnt lgkmcnt(0)
	v_mfma_scale_f32_16x16x128_f8f6f4 v[92:95], v[0:7], v[172:179], v[92:95], v218, v219 op_sel_hi:[0,0,0]
	v_mfma_scale_f32_16x16x128_f8f6f4 v[88:91], v[8:15], v[172:179], v[88:91], v218, v219 op_sel_hi:[0,0,0]
	v_mfma_scale_f32_16x16x128_f8f6f4 v[76:79], v[0:7], v[226:233], v[76:79], v218, v219 op_sel_hi:[0,0,0]
	v_mfma_scale_f32_16x16x128_f8f6f4 v[72:75], v[8:15], v[226:233], v[72:75], v218, v219 op_sel_hi:[0,0,0]
	v_mfma_scale_f32_16x16x128_f8f6f4 v[60:63], v[0:7], v[234:241], v[60:63], v218, v219 op_sel_hi:[0,0,0]
	v_mfma_scale_f32_16x16x128_f8f6f4 v[56:59], v[8:15], v[234:241], v[56:59], v218, v219 op_sel_hi:[0,0,0]
	v_mfma_scale_f32_16x16x128_f8f6f4 v[44:47], v[0:7], v[242:249], v[44:47], v218, v219 op_sel_hi:[0,0,0]
	v_mfma_scale_f32_16x16x128_f8f6f4 v[40:43], v[8:15], v[242:249], v[40:43], v218, v219 op_sel_hi:[0,0,0]
	s_setprio 0
	s_setprio 1
	v_mfma_scale_f32_16x16x128_f8f6f4 v[84:87], v[16:23], v[172:179], v[84:87], v218, v219 op_sel_hi:[0,0,0]
	v_mfma_scale_f32_16x16x128_f8f6f4 v[80:83], v[24:31], v[172:179], v[80:83], v218, v219 op_sel_hi:[0,0,0]
	v_mfma_scale_f32_16x16x128_f8f6f4 v[68:71], v[16:23], v[226:233], v[68:71], v218, v219 op_sel_hi:[0,0,0]
	v_mfma_scale_f32_16x16x128_f8f6f4 v[64:67], v[24:31], v[226:233], v[64:67], v218, v219 op_sel_hi:[0,0,0]
	v_mfma_scale_f32_16x16x128_f8f6f4 v[52:55], v[16:23], v[234:241], v[52:55], v218, v219 op_sel_hi:[0,0,0]
	v_mfma_scale_f32_16x16x128_f8f6f4 v[48:51], v[24:31], v[234:241], v[48:51], v218, v219 op_sel_hi:[0,0,0]
	v_mfma_scale_f32_16x16x128_f8f6f4 v[36:39], v[16:23], v[242:249], v[36:39], v218, v219 op_sel_hi:[0,0,0]
	v_mfma_scale_f32_16x16x128_f8f6f4 v[32:35], v[24:31], v[242:249], v[32:35], v218, v219 op_sel_hi:[0,0,0]
	s_setprio 0
	s_barrier
	s_add_u32 s2, s2, 0x100
	s_addc_u32 s3, s3, 0
	s_add_u32 s57, s57, 0x100
	s_addc_u32 s82, s82, 0
	s_cmp_ge_i32 s83, s91
	s_cselect_b32 s99, 0, 1
	s_mov_b32 s78, s83
	s_cbranch_scc0 .LBB0_1658
